# gather: next token PLE/Z rows and token-after-next IDX/GW prefetched into dead VGPRs (no exposed HBM round trips per token)
# speedup vs baseline: 1.0557x; 1.0047x over previous
; __device__ __forceinline__ int fresh_lane() { unsigned z = 0u; asm volatile("" : "+v"(z)); return (int)__builtin_amdgcn_mbcnt_hi(~0u, __builtin_amdgcn_mbcnt_lo(~0u, z)); }
; #define GATHER_ISSUE(k, sn_) do { const int sn = (sn_); const int secn = (sn >> 6) & 3; \
;         const int idsel = (sn >= 256) ? id0n : ((secn & 1) ? id1 : id0); \
;         const unsigned so = (unsigned)__builtin_amdgcn_readlane(idsel, sn & 63) * ROW4 + ((secn >= 2) ? TAB4 : 0u); \
;         ring[k] = __builtin_bit_cast(v4u, __builtin_amdgcn_raw_buffer_load_b128(rs, voff, so, 0)); } while (0)
;     const unsigned char* UV4 = (const unsigned char*)(F.ws + WS_UB) + (size_t)layer * (2u * TAB4);
;     const bf16* ZB = (const bf16*)(F.ws + WS_ZF); const bf16* PLE = (const bf16*)(F.ws + WS_PLE);
;     const int* IDX = (const int*)(F.ws + WS_IDX); const float* GWt = (const float*)(F.ws + WS_GW);
;     float* OF = (layer == 3 && !dummy) ? F.out : (float*)nullptr; bf16* XB = (bf16*)(F.ws + (dummy ? WS_X1B : WS_XB));
;     ...
;     const int idmask = (dummy == 1) ? PROBE_GATHER_MASK : 0x3fff;
;     ...
;     const float* gain1 = F.ln_gain + (size_t)(layer * 2) * D; const float* bias1 = F.ln_bias + (size_t)(layer * 2) * D;
;     const float* gain = F.ln_gain + (size_t)(layer * 2 + 1) * D; const float* bias = F.ln_bias + (size_t)(layer * 2 + 1) * D;
;     const int lane = fresh_lane();
;     const bool b3 = (lane & 8) != 0, b2 = (lane & 4) != 0, b1 = (lane & 2) != 0, b0 = (lane & 1) != 0;
;     const __amdgpu_buffer_rsrc_t rs = __builtin_amdgcn_make_buffer_rsrc((void*)UV4, (short)0, (int)(2u * TAB4), 0x00020000);
;     const unsigned voff = (unsigned)lane * 16u;
;     v4u ring[16];
;     int id0 = 0, id1 = 0, id0n = 0;
;     ...
;     int id1n = 0; float g0n = 0.f, g1n = 0.f;
;     if (F.gw < T) { gather_sorted_ids(IDX, GWt, F.gw, lane, id0n, id1n, g0n, g1n);
;     ...
;         id0n &= idmask; id1n &= idmask;
;     ...
; #pragma unroll
;         for (int k = 0; k < 16; ++k) GATHER_ISSUE(k, 256 + k); }
.LBB0_1412:
	s_andn2_b64 vcc, exec, s[14:15]
	s_cbranch_vccnz .LBB0_1452
	s_add_u32 s8, s60, 0x4a600000
	v_writelane_b32 v254, s8, 56
	s_addc_u32 s8, s61, 0
	v_writelane_b32 v255, s8, 5
	s_add_u32 s8, s60, 0x66600000
	v_writelane_b32 v255, s8, 7
	s_addc_u32 s8, s61, 0
	s_cmp_eq_u32 s18, 3
	v_writelane_b32 v255, s8, 9
	s_cselect_b64 s[8:9], -1, 0
	s_add_u32 s10, s60, 0x36600000
	v_writelane_b32 v255, s10, 11
	s_addc_u32 s43, s61, 0
	s_lshl_b32 s10, s18, 1
	s_mov_b64 s[16:17], s[80:81]
	v_writelane_b32 v255, s76, 1
	s_mov_b64 s[18:19], s[82:83]
	s_mov_b64 s[20:21], s[84:85]
	s_mov_b64 s[22:23], s[86:87]
	v_writelane_b32 v255, s77, 2
	v_readlane_b32 s76, v254, 1
	s_ashr_i32 s11, s10, 31
	v_readlane_b32 s90, v254, 15
	v_readlane_b32 s91, v254, 16
	s_lshl_b64 s[12:13], s[10:11], 13
	s_mov_b64 s[14:15], s[90:91]
	s_add_u32 s36, s14, s12
	s_addc_u32 s37, s15, s13
	s_add_u32 s12, s16, s12
	s_addc_u32 s13, s17, s13
	s_or_b32 s10, s10, 1
	v_readlane_b32 s72, v255, 1
	s_ashr_i32 s11, s10, 31
	v_readlane_b32 s73, v255, 2
	v_writelane_b32 v255, s12, 13
	s_lshl_b64 s[10:11], s[10:11], 13
	v_readlane_b32 s80, v254, 5
	v_writelane_b32 v255, s13, 14
	s_add_u32 s12, s14, s10
	s_addc_u32 s13, s15, s11
	v_readlane_b32 s81, v254, 6
	s_add_u32 s80, s16, s10
	s_addc_u32 s81, s17, s11
	v_readlane_b32 s10, v254, 51
	v_readlane_b32 s82, v254, 7
	v_readlane_b32 s83, v254, 8
	v_readlane_b32 s11, v254, 52
	s_and_b64 s[82:83], s[8:9], s[10:11]
	s_add_u32 s30, s60, 0x57600000
	v_writelane_b32 v255, s12, 15
	s_addc_u32 s39, s61, 0
	s_add_u32 s8, s60, 0x53200000
	v_writelane_b32 v255, s13, 16
	v_writelane_b32 v255, s8, 33
	s_addc_u32 s8, s61, 0
	v_writelane_b32 v255, s8, 35
	s_add_u32 s8, s60, 0x53600000
	v_writelane_b32 v255, s8, 29
	s_addc_u32 s8, s61, 0
	v_cmp_eq_u32_e64 s[28:29], 0, v68
	v_cmp_eq_u32_e32 vcc, 0, v67
	v_writelane_b32 v255, s8, 31
	s_xor_b64 s[44:45], vcc, s[28:29]
	v_cmp_eq_u32_e64 s[20:21], 0, v69
	v_writelane_b32 v255, s44, 17
	v_lshlrev_b32_e32 v70, 5, v130
	v_ashrrev_i32_e32 v71, 31, v70
	v_writelane_b32 v255, s45, 18
	s_xor_b64 s[44:45], vcc, s[20:21]
	v_writelane_b32 v255, s44, 19
	v_add_u32_e32 v194, 4, v66
	v_add_u32_e32 v195, 8, v66
	v_writelane_b32 v255, s45, 20
	s_xor_b64 s[44:45], vcc, s[0:1]
	v_writelane_b32 v255, s44, 21
	v_add_u32_e32 v196, 12, v66
	v_lshl_add_u64 v[66:67], s[60:61], 0, v[70:71]
	v_writelane_b32 v255, s45, 22
	s_xor_b64 s[44:45], vcc, s[2:3]
	v_writelane_b32 v255, s44, 23
	s_xor_b64 s[8:9], s[4:5], s[6:7]
	s_xor_b64 s[10:11], s[2:3], s[4:5]
	v_writelane_b32 v255, s45, 24
	s_xor_b64 s[44:45], vcc, s[4:5]
	v_writelane_b32 v255, s44, 25
	s_xor_b64 s[12:13], s[2:3], s[6:7]
	s_xor_b64 s[14:15], s[0:1], s[2:3]
	v_writelane_b32 v255, s45, 26
	s_xor_b64 s[44:45], vcc, s[6:7]
	v_writelane_b32 v255, s44, 27
	s_xor_b64 s[16:17], s[0:1], s[4:5]
	s_xor_b64 s[18:19], s[0:1], s[6:7]
	v_writelane_b32 v255, s45, 28
	s_mov_b64 s[44:45], 0x55600000
	s_xor_b64 s[22:23], s[20:21], s[0:1]
	s_xor_b64 s[24:25], s[20:21], s[2:3]
	s_xor_b64 s[26:27], s[20:21], s[4:5]
	v_ashrrev_i32_e32 v193, 4, v130
	v_lshl_add_u64 v[132:133], v[66:67], 0, s[44:45]
	s_xor_b64 s[44:45], s[20:21], s[6:7]
	s_xor_b64 s[46:47], s[28:29], s[20:21]
	s_xor_b64 s[48:49], s[28:29], s[0:1]
	s_xor_b64 s[50:51], s[28:29], s[2:3]
	s_xor_b64 s[52:53], s[28:29], s[4:5]
	s_xor_b64 s[54:55], s[28:29], s[6:7]
	v_readlane_b32 s77, v254, 2
	v_readlane_b32 s78, v254, 3
	v_readlane_b32 s79, v254, 4
	v_readlane_b32 s84, v254, 9
	v_readlane_b32 s85, v254, 10
	v_readlane_b32 s86, v254, 11
	v_readlane_b32 s87, v254, 12
	v_readlane_b32 s88, v254, 13
	v_readlane_b32 s89, v254, 14
	v_readlane_b32 s98, v254, 55
	s_lshl_b32 s98, s98, 6
	v_add_u32_e32 v228, s98, v130
	v_lshlrev_b32_e32 v228, 4, v228
	global_load_dwordx4 v[212:215], v228, s[36:37]
	global_load_dwordx4 v[224:227], v228, s[80:81]
	v_readlane_b32 s98, v255, 13
	v_readlane_b32 s99, v255, 14
	s_nop 4
	global_load_dwordx4 v[216:219], v228, s[98:99]
	v_readlane_b32 s98, v255, 15
	v_readlane_b32 s99, v255, 16
	s_nop 4
	global_load_dwordx4 v[220:223], v228, s[98:99]
	s_waitcnt vmcnt(3)
	ds_write_b128 v228, v[212:215]
	s_waitcnt vmcnt(2)
	ds_write_b128 v228, v[224:227] offset:24576
	s_waitcnt vmcnt(1)
	ds_write_b128 v228, v[216:219] offset:8192
	s_waitcnt vmcnt(0)
	ds_write_b128 v228, v[220:223] offset:16384
	s_waitcnt lgkmcnt(0)
	s_barrier
	v_readlane_b32 s100, v254, 58
	v_readlane_b32 s99, v255, 1
	s_add_i32 s99, s100, s99
	s_cmp_lt_i32 s99, 0x4000
	s_cselect_b32 s99, s99, s100
	s_lshl_b32 s100, s100, 12
	s_lshl_b32 s99, s99, 9
	v_lshl_add_u32 v244, v130, 6, s100
	v_lshl_add_u32 v249, v130, 2, s99
	v_readlane_b32 s100, v255, 7
	v_readlane_b32 s101, v255, 9
	s_nop 4
	global_load_dwordx4 v[212:215], v244, s[100:101] offset:48
	global_load_dwordx4 v[216:219], v244, s[100:101] offset:32
	global_load_dwordx4 v[220:223], v244, s[100:101] offset:16
	global_load_dwordx4 v[224:227], v244, s[100:101]
	v_readlane_b32 s100, v254, 56
	v_readlane_b32 s101, v255, 5
	s_nop 4
	global_load_dwordx4 v[228:231], v244, s[100:101] offset:48
	global_load_dwordx4 v[232:235], v244, s[100:101] offset:32
	global_load_dwordx4 v[236:239], v244, s[100:101] offset:16
	global_load_dwordx4 v[240:243], v244, s[100:101]
	global_load_dword v245, v249, s[70:71] offset:256
	global_load_dword v246, v249, s[40:41] offset:256
	global_load_dword v247, v249, s[40:41]
	global_load_dword v248, v249, s[70:71]
	s_branch .LBB0_1416

; __device__ __forceinline__ int shx_i(int v, int m, int lane) { return __builtin_amdgcn_ds_bpermute((lane ^ m) << 2, v); }
; __device__ __forceinline__ void gather_sorted_ids(const int* IDX, const float* GWt, int t, int lane, int& id0, int& id1, float& g0, float& g1) {
;     const int ia = IDX[(size_t)t * 128 + lane], ib = IDX[(size_t)t * 128 + 64 + lane];
;     const float ga = GWt[(size_t)t * 128 + lane], gb = GWt[(size_t)t * 128 + 64 + lane];
;     unsigned a = ((unsigned)ia << 16) | (unsigned)fminf(ga * 65536.0f, 65535.0f), b = ((unsigned)ib << 16) | (unsigned)fminf(gb * 65536.0f, 65535.0f);
; #pragma unroll
;     for (int k = 2; k <= 128; k <<= 1) {
;         if (k == 128) { const unsigned mn = a < b ? a : b, mx = a < b ? b : a; a = mn; b = mx; }
; #pragma unroll
;         for (int j = (k >= 128 ? 32 : k >> 1); j > 0; j >>= 1) {
;             const bool lower = (lane & j) == 0;
;             const bool upa = (k >= 128) ? true : ((lane & k) == 0);
;             const bool upb = (k >= 128) ? true : (k == 64 ? false : ((lane & k) == 0));
;             const unsigned oa = (unsigned)shx_i((int)a, j, lane), ob = (unsigned)shx_i((int)b, j, lane);
;             a = (lower == upa) ? (a < oa ? a : oa) : (a < oa ? oa : a);
;             b = (lower == upb) ? (b < ob ? b : ob) : (b < ob ? ob : b);
;         }
;     }
;     ...
;     for (int t = F.gw; t < T; t += F.ngw) {
;         int xh[4], xl[4]; float xdq, mean1, rstd1;
;         {
;             const v4u hq = *(const v4u*)(F.ws + WS_XQ + (size_t)t * 2048 + lane * 32), lq = *(const v4u*)(F.ws + WS_XQ + (size_t)t * 2048 + lane * 32 + 16);
;             const f32x4 r4 = *(const f32x4*)(F.ws + WS_R4 + (size_t)t * 16);
;             xh[0] = (int)hq.x; xh[1] = (int)hq.y; xh[2] = (int)hq.z; xh[3] = (int)hq.w; xl[0] = (int)lq.x; xl[1] = (int)lq.y; xl[2] = (int)lq.z; xl[3] = (int)lq.w;
;             xdq = r4[0]; mean1 = r4[1]; rstd1 = r4[2];
;         }
;         if (t - F.wave + (NWAVES - 1) < T) __syncthreads();
;         id0 = id0n; id1 = id1n; const float g0 = g0n, g1 = g1n;
;         { const int tn = (t + F.ngw < T) ? t + F.ngw : t; gather_sorted_ids(IDX, GWt, tn, lane, id0n, id1n, g0n, g1n);
.LBB0_1416:
	v_readlane_b32 s62, v254, 58
	s_ashr_i32 s89, s62, 31
	s_mov_b32 s88, s62
	s_lshl_b64 s[86:87], s[88:89], 11
	s_lshl_b64 s[56:57], s[88:89], 4
	v_lshl_add_u64 v[66:67], v[132:133], 0, s[86:87]
	s_add_u32 s56, s30, s56
	global_load_dwordx4 v[70:73], v[66:67], off offset:16
	s_addc_u32 s57, s39, s57
	global_load_dwordx4 v[74:77], v[66:67], off
	s_nop 0
	global_load_dwordx3 v[66:68], v1, s[56:57]
	v_readlane_b32 s56, v254, 55
	s_sub_i32 s56, s62, s56
	s_cmpk_gt_i32 s56, 0x3ff8
	v_readlane_b32 s63, v254, 59
	s_cbranch_scc1 .LBB0_1418
	s_waitcnt lgkmcnt(0)
	s_barrier
.LBB0_1418:
	s_add_i32 s62, s88, s72
	s_cmpk_gt_i32 s62, 0x3fff
	s_mov_b32 s56, s62
	s_cselect_b64 s[84:85], -1, 0
	s_cmpk_lt_i32 s62, 0x4000
	v_writelane_b32 v254, s56, 58
	s_nop 1
	v_writelane_b32 v254, s57, 59
	s_cselect_b32 s56, s62, s88
	s_ashr_i32 s57, s56, 31
	s_lshl_b64 s[56:57], s[56:57], 7
	v_lshl_add_u64 v[84:85], s[56:57], 0, v[130:131]
	v_lshlrev_b64 v[84:85], 2, v[84:85]
	s_mov_b64 s[56:57], 0x100
	v_lshl_add_u64 v[86:87], v[84:85], 0, s[56:57]
	v_lshl_add_u64 v[88:89], s[70:71], 0, v[86:87]
	v_lshl_add_u64 v[86:87], s[40:41], 0, v[86:87]
	s_waitcnt vmcnt(3)
	v_mov_b32_e32 v69, v245
	v_mov_b32_e32 v81, v246
	v_lshl_add_u64 v[86:87], s[70:71], 0, v[84:85]
	v_lshl_add_u64 v[84:85], s[40:41], 0, v[84:85]
	v_readlane_b32 s56, v255, 17
	v_readlane_b32 s57, v255, 18
	v_mov_b32_e32 v83, v247
	v_mul_f32_e32 v81, 0x47800000, v81
	v_min_f32_e32 v81, 0x477fff00, v81
	v_cvt_u32_f32_e32 v81, v81
	v_mul_f32_e32 v83, 0x47800000, v83
	v_lshl_or_b32 v69, v69, 16, v81
	v_mov_b32_e32 v81, v248
	ds_bpermute_b32 v84, v163, v69
	v_min_f32_e32 v83, 0x477fff00, v83
	v_cvt_u32_f32_e32 v83, v83
	v_lshl_or_b32 v81, v81, 16, v83
	ds_bpermute_b32 v83, v163, v81
	s_waitcnt lgkmcnt(0)
	v_min_u32_e32 v85, v81, v83
	v_max_u32_e32 v81, v81, v83
	v_min_u32_e32 v83, v69, v84
	v_max_u32_e32 v69, v69, v84
	v_cndmask_b32_e64 v81, v85, v81, s[8:9]
	v_cndmask_b32_e64 v69, v83, v69, s[8:9]
	ds_bpermute_b32 v83, v188, v81
	ds_bpermute_b32 v84, v188, v69
	s_waitcnt lgkmcnt(1)
	v_min_u32_e32 v85, v81, v83
	v_max_u32_e32 v81, v81, v83
	s_waitcnt lgkmcnt(0)
	v_min_u32_e32 v83, v69, v84
	v_max_u32_e32 v69, v69, v84
	v_cndmask_b32_e64 v81, v85, v81, s[10:11]
	v_cndmask_b32_e64 v69, v83, v69, s[10:11]
	ds_bpermute_b32 v83, v163, v81
	ds_bpermute_b32 v84, v163, v69
	s_waitcnt lgkmcnt(1)
	v_min_u32_e32 v85, v81, v83
	v_max_u32_e32 v81, v81, v83
	s_waitcnt lgkmcnt(0)
	v_min_u32_e32 v83, v69, v84
	v_max_u32_e32 v69, v69, v84
	v_cndmask_b32_e64 v81, v85, v81, s[12:13]
	v_cndmask_b32_e64 v69, v83, v69, s[12:13]
	ds_bpermute_b32 v83, v189, v81
	ds_bpermute_b32 v84, v189, v69
	s_waitcnt lgkmcnt(1)
	v_min_u32_e32 v85, v81, v83
	v_max_u32_e32 v81, v81, v83
	s_waitcnt lgkmcnt(0)
	v_min_u32_e32 v83, v69, v84
	v_max_u32_e32 v69, v69, v84
	v_cndmask_b32_e64 v81, v85, v81, s[14:15]
	v_cndmask_b32_e64 v69, v83, v69, s[14:15]
	ds_bpermute_b32 v83, v188, v81
	ds_bpermute_b32 v84, v188, v69
	s_waitcnt lgkmcnt(1)
	v_min_u32_e32 v85, v81, v83
	v_max_u32_e32 v81, v81, v83
	s_waitcnt lgkmcnt(0)
	v_min_u32_e32 v83, v69, v84
	v_max_u32_e32 v69, v69, v84
	v_cndmask_b32_e64 v81, v85, v81, s[16:17]
	v_cndmask_b32_e64 v69, v83, v69, s[16:17]
	ds_bpermute_b32 v83, v163, v81
	ds_bpermute_b32 v84, v163, v69
	s_waitcnt lgkmcnt(1)
	v_min_u32_e32 v85, v81, v83
	v_max_u32_e32 v81, v81, v83
	s_waitcnt lgkmcnt(0)
	v_min_u32_e32 v83, v69, v84
	v_max_u32_e32 v69, v69, v84
	v_cndmask_b32_e64 v81, v85, v81, s[18:19]
	v_cndmask_b32_e64 v69, v83, v69, s[18:19]
	ds_bpermute_b32 v83, v190, v81
	ds_bpermute_b32 v84, v190, v69
	s_waitcnt lgkmcnt(1)
	v_min_u32_e32 v85, v81, v83
	v_max_u32_e32 v81, v81, v83
	s_waitcnt lgkmcnt(0)
	v_min_u32_e32 v83, v69, v84
	v_max_u32_e32 v69, v69, v84
	v_cndmask_b32_e64 v81, v85, v81, s[22:23]
	v_cndmask_b32_e64 v69, v83, v69, s[22:23]
	ds_bpermute_b32 v83, v189, v81
	ds_bpermute_b32 v84, v189, v69
	s_waitcnt lgkmcnt(1)
	v_min_u32_e32 v85, v81, v83
	v_max_u32_e32 v81, v81, v83
	s_waitcnt lgkmcnt(0)
	v_min_u32_e32 v83, v69, v84
	v_max_u32_e32 v69, v69, v84
	v_cndmask_b32_e64 v81, v85, v81, s[24:25]
	v_cndmask_b32_e64 v69, v83, v69, s[24:25]
	ds_bpermute_b32 v83, v188, v81
	ds_bpermute_b32 v84, v188, v69
	s_waitcnt lgkmcnt(1)
	v_min_u32_e32 v85, v81, v83
	v_max_u32_e32 v81, v81, v83
	s_waitcnt lgkmcnt(0)
	v_min_u32_e32 v83, v69, v84
	v_max_u32_e32 v69, v69, v84
	v_cndmask_b32_e64 v81, v85, v81, s[26:27]
	v_cndmask_b32_e64 v69, v83, v69, s[26:27]
	ds_bpermute_b32 v83, v163, v81
	ds_bpermute_b32 v84, v163, v69
	s_waitcnt lgkmcnt(1)
	v_min_u32_e32 v85, v81, v83
	v_max_u32_e32 v81, v81, v83
	s_waitcnt lgkmcnt(0)
	v_min_u32_e32 v83, v69, v84
	v_max_u32_e32 v69, v69, v84
	v_cndmask_b32_e64 v81, v85, v81, s[44:45]
	v_cndmask_b32_e64 v69, v83, v69, s[44:45]
	ds_bpermute_b32 v83, v191, v81
	ds_bpermute_b32 v84, v191, v69
	s_waitcnt lgkmcnt(1)
	v_min_u32_e32 v85, v81, v83
	v_max_u32_e32 v81, v81, v83
	s_waitcnt lgkmcnt(0)
	v_min_u32_e32 v83, v69, v84
	v_max_u32_e32 v69, v69, v84
	v_cndmask_b32_e64 v81, v85, v81, s[46:47]
	v_cndmask_b32_e64 v69, v83, v69, s[46:47]
	ds_bpermute_b32 v83, v190, v81
	ds_bpermute_b32 v84, v190, v69
	s_waitcnt lgkmcnt(1)
; __device__ __forceinline__ int shx_i(int v, int m, int lane) { return __builtin_amdgcn_ds_bpermute((lane ^ m) << 2, v); }
; __device__ __forceinline__ void gather_sorted_ids(const int* IDX, const float* GWt, int t, int lane, int& id0, int& id1, float& g0, float& g1) {
;     ...
; #pragma unroll
;     for (int k = 2; k <= 128; k <<= 1) {
;         if (k == 128) { const unsigned mn = a < b ? a : b, mx = a < b ? b : a; a = mn; b = mx; }
; #pragma unroll
;         for (int j = (k >= 128 ? 32 : k >> 1); j > 0; j >>= 1) {
;             const bool lower = (lane & j) == 0;
;             const bool upa = (k >= 128) ? true : ((lane & k) == 0);
;             const bool upb = (k >= 128) ? true : (k == 64 ? false : ((lane & k) == 0));
;             const unsigned oa = (unsigned)shx_i((int)a, j, lane), ob = (unsigned)shx_i((int)b, j, lane);
;             a = (lower == upa) ? (a < oa ? a : oa) : (a < oa ? oa : a);
;             b = (lower == upb) ? (b < ob ? b : ob) : (b < ob ? ob : b);
;         }
;     }
;     id0 = (int)(a >> 16); id1 = (int)(b >> 16);
;     g0 = ((float)(a & 0xffffu) + 0.5f) * (1.0f / 65536.0f); g1 = ((float)(b & 0xffffu) + 0.5f) * (1.0f / 65536.0f);
; }
	v_min_u32_e32 v85, v81, v83
	v_max_u32_e32 v81, v81, v83
	s_waitcnt lgkmcnt(0)
	v_min_u32_e32 v83, v69, v84
	v_max_u32_e32 v69, v69, v84
	v_cndmask_b32_e64 v81, v85, v81, s[48:49]
	v_cndmask_b32_e64 v69, v83, v69, s[48:49]
	ds_bpermute_b32 v83, v189, v81
	ds_bpermute_b32 v84, v189, v69
	s_waitcnt lgkmcnt(1)
	v_min_u32_e32 v85, v81, v83
	v_max_u32_e32 v81, v81, v83
	s_waitcnt lgkmcnt(0)
	v_min_u32_e32 v83, v69, v84
	v_max_u32_e32 v69, v69, v84
	v_cndmask_b32_e64 v81, v85, v81, s[50:51]
	v_cndmask_b32_e64 v69, v83, v69, s[50:51]
	ds_bpermute_b32 v83, v188, v81
	ds_bpermute_b32 v84, v188, v69
	s_waitcnt lgkmcnt(1)
	v_min_u32_e32 v85, v81, v83
	v_max_u32_e32 v81, v81, v83
	s_waitcnt lgkmcnt(0)
	v_min_u32_e32 v83, v69, v84
	v_max_u32_e32 v69, v69, v84
	v_cndmask_b32_e64 v81, v85, v81, s[52:53]
	v_cndmask_b32_e64 v69, v83, v69, s[52:53]
	ds_bpermute_b32 v83, v163, v81
	ds_bpermute_b32 v84, v163, v69
	s_waitcnt lgkmcnt(1)
	v_min_u32_e32 v85, v81, v83
	v_max_u32_e32 v81, v81, v83
	s_waitcnt lgkmcnt(0)
	v_min_u32_e32 v83, v69, v84
	v_max_u32_e32 v69, v69, v84
	v_cndmask_b32_e64 v81, v85, v81, s[54:55]
	v_cndmask_b32_e64 v69, v83, v69, s[54:55]
	ds_bpermute_b32 v83, v192, v81
	ds_bpermute_b32 v84, v192, v69
	s_waitcnt lgkmcnt(1)
	v_min_u32_e32 v85, v81, v83
	v_max_u32_e32 v81, v81, v83
	s_waitcnt lgkmcnt(0)
	v_min_u32_e32 v83, v69, v84
	v_max_u32_e32 v69, v69, v84
	v_cndmask_b32_e64 v81, v85, v81, s[56:57]
	v_cndmask_b32_e64 v69, v83, v69, s[28:29]
	ds_bpermute_b32 v83, v191, v81
	ds_bpermute_b32 v84, v191, v69
	v_readlane_b32 s56, v255, 19
	v_readlane_b32 s57, v255, 20
	s_waitcnt lgkmcnt(1)
	v_min_u32_e32 v85, v81, v83
	v_max_u32_e32 v81, v81, v83
	s_waitcnt lgkmcnt(0)
	v_min_u32_e32 v83, v69, v84
	v_max_u32_e32 v69, v69, v84
	v_cndmask_b32_e64 v81, v85, v81, s[56:57]
	v_cndmask_b32_e64 v69, v83, v69, s[20:21]
	ds_bpermute_b32 v83, v190, v81
	ds_bpermute_b32 v84, v190, v69
	v_readlane_b32 s56, v255, 21
	v_readlane_b32 s57, v255, 22
	s_waitcnt lgkmcnt(1)
	v_min_u32_e32 v85, v81, v83
	v_max_u32_e32 v81, v81, v83
	s_waitcnt lgkmcnt(0)
	v_min_u32_e32 v83, v69, v84
	v_max_u32_e32 v69, v69, v84
	v_cndmask_b32_e64 v81, v85, v81, s[56:57]
	v_cndmask_b32_e64 v69, v83, v69, s[0:1]
	ds_bpermute_b32 v83, v189, v81
	ds_bpermute_b32 v84, v189, v69
	v_readlane_b32 s56, v255, 23
	v_readlane_b32 s57, v255, 24
	s_waitcnt lgkmcnt(1)
	v_min_u32_e32 v85, v81, v83
	v_max_u32_e32 v81, v81, v83
	s_waitcnt lgkmcnt(0)
	v_min_u32_e32 v83, v69, v84
	v_max_u32_e32 v69, v69, v84
	v_cndmask_b32_e64 v81, v85, v81, s[56:57]
	v_cndmask_b32_e64 v69, v83, v69, s[2:3]
	ds_bpermute_b32 v83, v188, v81
	ds_bpermute_b32 v84, v188, v69
	v_readlane_b32 s56, v255, 25
	v_readlane_b32 s57, v255, 26
	s_waitcnt lgkmcnt(1)
	v_min_u32_e32 v85, v81, v83
	v_max_u32_e32 v81, v81, v83
	s_waitcnt lgkmcnt(0)
	v_min_u32_e32 v83, v69, v84
	v_max_u32_e32 v69, v69, v84
	v_cndmask_b32_e64 v81, v85, v81, s[56:57]
	v_cndmask_b32_e64 v69, v83, v69, s[4:5]
	ds_bpermute_b32 v83, v163, v81
	ds_bpermute_b32 v84, v163, v69
	v_readlane_b32 s56, v255, 27
	v_readlane_b32 s57, v255, 28
	s_waitcnt lgkmcnt(1)
	v_max_u32_e32 v85, v81, v83
	v_min_u32_e32 v81, v81, v83
	s_waitcnt lgkmcnt(0)
	v_max_u32_e32 v83, v69, v84
	v_min_u32_e32 v69, v69, v84
	v_cndmask_b32_e64 v81, v81, v85, s[56:57]
	v_cndmask_b32_e64 v69, v69, v83, s[6:7]
	v_max_u32_e32 v83, v81, v69
	v_min_u32_e32 v69, v81, v69
	ds_bpermute_b32 v81, v192, v69
	ds_bpermute_b32 v84, v192, v83
	s_mov_b32 s56, 0
	s_mov_b32 s57, 31
	s_waitcnt lgkmcnt(1)
	v_min_u32_e32 v85, v69, v81
	v_max_u32_e32 v69, v69, v81
	v_cndmask_b32_e64 v69, v69, v85, s[28:29]
	s_waitcnt lgkmcnt(0)
	v_min_u32_e32 v81, v83, v84
	v_max_u32_e32 v83, v83, v84
	v_cndmask_b32_e64 v81, v83, v81, s[28:29]
	ds_bpermute_b32 v83, v191, v69
	ds_bpermute_b32 v84, v191, v81
	s_waitcnt lgkmcnt(1)
	v_min_u32_e32 v85, v69, v83
	v_max_u32_e32 v69, v69, v83
	v_cndmask_b32_e64 v69, v69, v85, s[20:21]
	s_waitcnt lgkmcnt(0)
	v_min_u32_e32 v83, v81, v84
	v_max_u32_e32 v81, v81, v84
	v_cndmask_b32_e64 v81, v81, v83, s[20:21]
	ds_bpermute_b32 v83, v190, v69
	ds_bpermute_b32 v84, v190, v81
	s_waitcnt lgkmcnt(1)
	v_min_u32_e32 v85, v69, v83
	v_max_u32_e32 v69, v69, v83
	v_cndmask_b32_e64 v69, v69, v85, s[0:1]
	s_waitcnt lgkmcnt(0)
	v_min_u32_e32 v83, v81, v84
	v_max_u32_e32 v81, v81, v84
	v_cndmask_b32_e64 v81, v81, v83, s[0:1]
	ds_bpermute_b32 v83, v189, v69
	ds_bpermute_b32 v84, v189, v81
	s_waitcnt lgkmcnt(1)
	v_min_u32_e32 v85, v69, v83
	v_max_u32_e32 v69, v69, v83
	v_cndmask_b32_e64 v69, v69, v85, s[2:3]
	s_waitcnt lgkmcnt(0)
	v_min_u32_e32 v83, v81, v84
	v_max_u32_e32 v81, v81, v84
	v_cndmask_b32_e64 v81, v81, v83, s[2:3]
	ds_bpermute_b32 v83, v188, v69
	ds_bpermute_b32 v84, v188, v81
	s_waitcnt lgkmcnt(1)
	v_min_u32_e32 v85, v69, v83
	v_max_u32_e32 v69, v69, v83
	v_cndmask_b32_e64 v105, v69, v85, s[4:5]
	s_waitcnt lgkmcnt(0)
	v_min_u32_e32 v69, v81, v84
	v_max_u32_e32 v81, v81, v84
	v_cndmask_b32_e64 v197, v81, v69, s[4:5]
	ds_bpermute_b32 v106, v163, v105
	ds_bpermute_b32 v198, v163, v197
	v_mov_b32_e32 v81, 0
	s_waitcnt vmcnt(0)

.LBB0_1425:
	s_add_i32 s56, s63, 0xffffff21
	s_waitcnt vmcnt(5)
	v_perm_b32 v106, v14, v6, s67
	v_perm_b32 v6, v14, v6, s68
	s_waitcnt vmcnt(3)
	v_perm_b32 v14, v46, v30, s67
	v_readlane_b32 s56, v105, s56
	v_perm_b32 v30, v46, v30, s68
	v_perm_b32 v46, v14, v106, s69
	v_perm_b32 v14, v14, v106, s33
	v_perm_b32 v106, v30, v6, s69
	v_perm_b32 v6, v30, v6, s33
	v_dot4c_i32_i8_e32 v74, s56, v14
	v_and_b32_e32 v14, 0xf0f0f0f0, v14
	v_dot4c_i32_i8_e32 v70, s56, v14
	v_and_b32_e32 v14, 0xf0f0f0f0, v106
	v_dot4c_i32_i8_e32 v76, s56, v6
	v_and_b32_e32 v6, 0xf0f0f0f0, v6
	v_and_b32_e32 v30, 0xf0f0f0f0, v46
	v_dot4c_i32_i8_e32 v72, s56, v14
	v_dot4c_i32_i8_e32 v73, s56, v6
	v_perm_b32 v6, v15, v7, s67
	v_perm_b32 v14, v47, v31, s67
	v_dot4c_i32_i8_e32 v69, s56, v30
	v_perm_b32 v7, v15, v7, s68
	v_perm_b32 v15, v47, v31, s68
	v_perm_b32 v30, v14, v6, s69
	v_perm_b32 v6, v14, v6, s33
	v_perm_b32 v14, v15, v7, s69
	v_dot4c_i32_i8_e32 v85, s56, v6
	v_and_b32_e32 v6, 0xf0f0f0f0, v6
	v_perm_b32 v7, v15, v7, s33
	v_dot4c_i32_i8_e32 v81, s56, v6
	v_and_b32_e32 v6, 0xf0f0f0f0, v14
	v_dot4c_i32_i8_e32 v82, s56, v6
	v_and_b32_e32 v6, 0xf0f0f0f0, v7
	v_and_b32_e32 v15, 0xf0f0f0f0, v30
	v_dot4c_i32_i8_e32 v94, s56, v7
	v_dot4c_i32_i8_e32 v84, s56, v6
	v_perm_b32 v6, v16, v8, s67
	v_perm_b32 v7, v16, v8, s68
	v_perm_b32 v8, v48, v32, s67
	v_dot4c_i32_i8_e32 v77, s56, v15
	v_dot4c_i32_i8_e32 v86, s56, v14
	v_perm_b32 v14, v48, v32, s68
	v_perm_b32 v15, v8, v6, s69
	v_perm_b32 v6, v8, v6, s33
	v_perm_b32 v8, v14, v7, s69
	v_dot4c_i32_i8_e32 v96, s56, v6
	v_and_b32_e32 v6, 0xf0f0f0f0, v6
	v_perm_b32 v7, v14, v7, s33
	v_dot4c_i32_i8_e32 v88, s56, v6
	v_and_b32_e32 v6, 0xf0f0f0f0, v8
	v_dot4c_i32_i8_e32 v89, s56, v6
	v_and_b32_e32 v6, 0xf0f0f0f0, v7
	v_and_b32_e32 v14, 0xf0f0f0f0, v15
	v_dot4c_i32_i8_e32 v97, s56, v8
	v_dot4c_i32_i8_e32 v90, s56, v6
	v_perm_b32 v6, v17, v9, s67
	v_perm_b32 v8, v49, v33, s67
	v_dot4c_i32_i8_e32 v87, s56, v14
	v_dot4c_i32_i8_e32 v98, s56, v7
	v_perm_b32 v7, v17, v9, s68
	v_perm_b32 v9, v49, v33, s68
	v_perm_b32 v14, v8, v6, s69
	v_perm_b32 v6, v8, v6, s33
	v_perm_b32 v8, v9, v7, s69
	v_dot4c_i32_i8_e32 v100, s56, v6
	v_and_b32_e32 v6, 0xf0f0f0f0, v6
	s_add_i32 s91, s63, -15
	v_perm_b32 v7, v9, v7, s33
	v_dot4c_i32_i8_e32 v92, s56, v6
	v_and_b32_e32 v6, 0xf0f0f0f0, v8
	s_cmp_gt_u32 s62, 2
	v_and_b32_e32 v9, 0xf0f0f0f0, v14
	v_dot4c_i32_i8_e32 v93, s56, v6
	v_and_b32_e32 v6, 0xf0f0f0f0, v7
	s_cselect_b64 vcc, -1, 0
	s_bitcmp0_b32 s91, 6
	v_dot4c_i32_i8_e32 v66, s56, v46
	v_dot4c_i32_i8_e32 v75, s56, v106
	v_dot4c_i32_i8_e32 v80, s56, v30
	v_dot4c_i32_i8_e32 v95, s56, v15
	v_dot4c_i32_i8_e32 v99, s56, v14
	v_dot4c_i32_i8_e32 v91, s56, v9
	v_dot4c_i32_i8_e32 v101, s56, v8
	v_dot4c_i32_i8_e32 v102, s56, v7
	v_dot4c_i32_i8_e32 v83, s56, v6
	s_cselect_b64 s[56:57], -1, 0
	v_cndmask_b32_e64 v6, v79, v78, s[56:57]
	v_cndmask_b32_e32 v6, v6, v199, vcc
	s_add_i32 s57, s90, 0xffe20000
	v_readlane_b32 s56, v6, s91
	s_lshl_b32 s56, s56, 10
	s_and_b32 s57, s57, 0x1000000
	s_add_i32 s56, s56, s57
	s_add_i32 s91, s63, -14
	s_bitcmp0_b32 s91, 6
	buffer_load_dwordx4 v[6:9], v0, s[92:95], s56 offen
	s_cselect_b64 s[56:57], -1, 0
	v_cndmask_b32_e64 v14, v79, v78, s[56:57]
	v_cndmask_b32_e32 v14, v14, v199, vcc
	s_add_i32 s57, s90, 0xffe40000
	v_readlane_b32 s56, v14, s91
	s_lshl_b32 s56, s56, 10
	s_and_b32 s57, s57, 0x1000000
	s_add_i32 s56, s56, s57
	s_add_i32 s91, s63, -13
	s_bitcmp0_b32 s91, 6
	buffer_load_dwordx4 v[14:17], v0, s[92:95], s56 offen
	s_cselect_b64 s[56:57], -1, 0
	v_cndmask_b32_e64 v30, v79, v78, s[56:57]
	v_cndmask_b32_e32 v30, v30, v199, vcc
	s_add_i32 s57, s90, 0xffe60000
	v_readlane_b32 s56, v30, s91
	s_lshl_b32 s56, s56, 10
	s_and_b32 s57, s57, 0x1000000
	s_add_i32 s56, s56, s57
	s_add_i32 s91, s63, -12
	s_bitcmp0_b32 s91, 6
	buffer_load_dwordx4 v[30:33], v0, s[92:95], s56 offen
	s_cselect_b64 s[56:57], -1, 0
	v_cndmask_b32_e64 v46, v79, v78, s[56:57]
	v_cndmask_b32_e32 v46, v46, v199, vcc
	s_add_i32 s57, s90, 0xffe80000
	v_readlane_b32 s56, v46, s91
	s_lshl_b32 s56, s56, 10
	s_and_b32 s57, s57, 0x1000000
	s_add_i32 s56, s56, s57
	s_nop 1
	buffer_load_dwordx4 v[46:49], v0, s[92:95], s56 offen
	s_add_i32 s56, s63, 0xffffff25
	s_waitcnt vmcnt(5)
	v_perm_b32 v106, v22, v2, s67
	v_perm_b32 v2, v22, v2, s68
	s_waitcnt vmcnt(3)
	v_perm_b32 v22, v54, v38, s67
	v_readlane_b32 s56, v105, s56
	v_perm_b32 v38, v54, v38, s68
	v_perm_b32 v54, v22, v106, s69
	v_perm_b32 v22, v22, v106, s33
	v_perm_b32 v106, v38, v2, s69
	v_perm_b32 v2, v38, v2, s33
	v_dot4c_i32_i8_e32 v74, s56, v22
	v_and_b32_e32 v22, 0xf0f0f0f0, v22
	v_dot4c_i32_i8_e32 v70, s56, v22
	v_and_b32_e32 v22, 0xf0f0f0f0, v106
	v_dot4c_i32_i8_e32 v76, s56, v2
	v_and_b32_e32 v2, 0xf0f0f0f0, v2
	v_and_b32_e32 v38, 0xf0f0f0f0, v54
	v_dot4c_i32_i8_e32 v72, s56, v22
	v_dot4c_i32_i8_e32 v73, s56, v2
	v_perm_b32 v2, v23, v3, s67
	v_perm_b32 v22, v55, v39, s67
	v_dot4c_i32_i8_e32 v69, s56, v38
	v_perm_b32 v3, v23, v3, s68
	v_perm_b32 v23, v55, v39, s68
	v_perm_b32 v38, v22, v2, s69
	v_perm_b32 v2, v22, v2, s33
	v_perm_b32 v22, v23, v3, s69
	v_dot4c_i32_i8_e32 v85, s56, v2
	v_and_b32_e32 v2, 0xf0f0f0f0, v2
	v_perm_b32 v3, v23, v3, s33
	v_dot4c_i32_i8_e32 v81, s56, v2
	v_and_b32_e32 v2, 0xf0f0f0f0, v22
	v_dot4c_i32_i8_e32 v82, s56, v2
	v_and_b32_e32 v2, 0xf0f0f0f0, v3
	v_and_b32_e32 v23, 0xf0f0f0f0, v38
	v_dot4c_i32_i8_e32 v94, s56, v3
	v_dot4c_i32_i8_e32 v84, s56, v2
	v_perm_b32 v2, v24, v4, s67
	v_perm_b32 v3, v24, v4, s68
	v_perm_b32 v4, v56, v40, s67
	v_dot4c_i32_i8_e32 v77, s56, v23
	v_dot4c_i32_i8_e32 v86, s56, v22
	v_perm_b32 v22, v56, v40, s68
	v_perm_b32 v23, v4, v2, s69
	v_perm_b32 v2, v4, v2, s33
	v_perm_b32 v4, v22, v3, s69
	v_dot4c_i32_i8_e32 v96, s56, v2
	v_and_b32_e32 v2, 0xf0f0f0f0, v2
	v_perm_b32 v3, v22, v3, s33
	v_dot4c_i32_i8_e32 v88, s56, v2
	v_and_b32_e32 v2, 0xf0f0f0f0, v4
	v_dot4c_i32_i8_e32 v89, s56, v2
	v_and_b32_e32 v2, 0xf0f0f0f0, v3
	v_and_b32_e32 v22, 0xf0f0f0f0, v23
	v_dot4c_i32_i8_e32 v97, s56, v4
	v_dot4c_i32_i8_e32 v90, s56, v2
	v_perm_b32 v2, v25, v5, s67
	v_perm_b32 v4, v57, v41, s67
	v_dot4c_i32_i8_e32 v87, s56, v22
	v_dot4c_i32_i8_e32 v98, s56, v3
	v_perm_b32 v3, v25, v5, s68
	v_perm_b32 v5, v57, v41, s68
	v_perm_b32 v22, v4, v2, s69
	v_perm_b32 v2, v4, v2, s33
	v_perm_b32 v4, v5, v3, s69
	v_dot4c_i32_i8_e32 v100, s56, v2
	v_and_b32_e32 v2, 0xf0f0f0f0, v2
	v_perm_b32 v3, v5, v3, s33
	v_dot4c_i32_i8_e32 v92, s56, v2
	v_and_b32_e32 v2, 0xf0f0f0f0, v4
	s_add_i32 s91, s63, -11
	v_and_b32_e32 v5, 0xf0f0f0f0, v22
	v_dot4c_i32_i8_e32 v93, s56, v2
	v_and_b32_e32 v2, 0xf0f0f0f0, v3
	s_bitcmp0_b32 s91, 6
	v_dot4c_i32_i8_e32 v66, s56, v54
	v_dot4c_i32_i8_e32 v75, s56, v106
	v_dot4c_i32_i8_e32 v80, s56, v38
	v_dot4c_i32_i8_e32 v95, s56, v23
	v_dot4c_i32_i8_e32 v99, s56, v22
	v_dot4c_i32_i8_e32 v91, s56, v5
	v_dot4c_i32_i8_e32 v101, s56, v4
	v_dot4c_i32_i8_e32 v102, s56, v3
	v_dot4c_i32_i8_e32 v83, s56, v2
	s_cselect_b64 s[56:57], -1, 0
	v_cndmask_b32_e64 v2, v79, v78, s[56:57]
	v_cndmask_b32_e32 v2, v2, v199, vcc
	s_add_i32 s57, s90, 0xffea0000
	v_readlane_b32 s56, v2, s91
	s_lshl_b32 s56, s56, 10
	s_and_b32 s57, s57, 0x1000000
	s_add_i32 s56, s56, s57
	s_add_i32 s91, s63, -10
	s_bitcmp0_b32 s91, 6
	buffer_load_dwordx4 v[2:5], v0, s[92:95], s56 offen
	s_cselect_b64 s[56:57], -1, 0
	v_cndmask_b32_e64 v22, v79, v78, s[56:57]
	v_cndmask_b32_e32 v22, v22, v199, vcc
	s_add_i32 s57, s90, 0xffec0000
	v_readlane_b32 s56, v22, s91
	s_lshl_b32 s56, s56, 10
	s_and_b32 s57, s57, 0x1000000
	s_add_i32 s56, s56, s57
	s_add_i32 s91, s63, -9
	s_bitcmp0_b32 s91, 6
	buffer_load_dwordx4 v[22:25], v0, s[92:95], s56 offen
	s_cselect_b64 s[56:57], -1, 0
	v_cndmask_b32_e64 v38, v79, v78, s[56:57]
	v_cndmask_b32_e32 v38, v38, v199, vcc
	s_add_i32 s57, s90, 0xffee0000
	v_readlane_b32 s56, v38, s91
	s_lshl_b32 s56, s56, 10
	s_and_b32 s57, s57, 0x1000000
	s_add_i32 s56, s56, s57
	s_add_i32 s91, s63, -8
	s_bitcmp0_b32 s91, 6
	buffer_load_dwordx4 v[38:41], v0, s[92:95], s56 offen
	s_cselect_b64 s[56:57], -1, 0
	v_cndmask_b32_e64 v54, v79, v78, s[56:57]
	v_cndmask_b32_e32 v54, v54, v199, vcc
	s_add_i32 s57, s90, 0xfff00000
	v_readlane_b32 s56, v54, s91
	s_lshl_b32 s56, s56, 10
	s_and_b32 s57, s57, 0x1000000
	s_add_i32 s56, s56, s57
	s_nop 1
	buffer_load_dwordx4 v[54:57], v0, s[92:95], s56 offen
	s_add_i32 s56, s63, 0xffffff29
	s_waitcnt vmcnt(5)
	v_perm_b32 v106, v26, v10, s67
	v_perm_b32 v10, v26, v10, s68
	s_waitcnt vmcnt(3)
	v_perm_b32 v26, v58, v42, s67
	v_readlane_b32 s56, v105, s56
	v_perm_b32 v42, v58, v42, s68
	v_perm_b32 v58, v26, v106, s69
	v_perm_b32 v26, v26, v106, s33
	v_perm_b32 v106, v42, v10, s69
	v_perm_b32 v10, v42, v10, s33
	v_dot4c_i32_i8_e32 v74, s56, v26
	v_and_b32_e32 v26, 0xf0f0f0f0, v26
	v_dot4c_i32_i8_e32 v70, s56, v26
	v_and_b32_e32 v26, 0xf0f0f0f0, v106
	v_dot4c_i32_i8_e32 v76, s56, v10
	v_and_b32_e32 v10, 0xf0f0f0f0, v10
	v_and_b32_e32 v42, 0xf0f0f0f0, v58
	v_dot4c_i32_i8_e32 v72, s56, v26
	v_dot4c_i32_i8_e32 v73, s56, v10
	v_perm_b32 v10, v27, v11, s67
	v_perm_b32 v26, v59, v43, s67
	v_dot4c_i32_i8_e32 v69, s56, v42
	v_perm_b32 v11, v27, v11, s68
	v_perm_b32 v27, v59, v43, s68
	v_perm_b32 v42, v26, v10, s69
	v_perm_b32 v10, v26, v10, s33
	v_perm_b32 v26, v27, v11, s69
	v_dot4c_i32_i8_e32 v85, s56, v10
	v_and_b32_e32 v10, 0xf0f0f0f0, v10
	v_perm_b32 v11, v27, v11, s33
	v_dot4c_i32_i8_e32 v81, s56, v10
	v_and_b32_e32 v10, 0xf0f0f0f0, v26
	v_dot4c_i32_i8_e32 v82, s56, v10
	v_and_b32_e32 v10, 0xf0f0f0f0, v11
	v_and_b32_e32 v27, 0xf0f0f0f0, v42
	v_dot4c_i32_i8_e32 v94, s56, v11
	v_dot4c_i32_i8_e32 v84, s56, v10
	v_perm_b32 v10, v28, v12, s67
	v_perm_b32 v11, v28, v12, s68
	v_perm_b32 v12, v60, v44, s67
	v_dot4c_i32_i8_e32 v77, s56, v27
	v_dot4c_i32_i8_e32 v86, s56, v26
	v_perm_b32 v26, v60, v44, s68
	v_perm_b32 v27, v12, v10, s69
	v_perm_b32 v10, v12, v10, s33
	v_perm_b32 v12, v26, v11, s69
	v_dot4c_i32_i8_e32 v96, s56, v10
	v_and_b32_e32 v10, 0xf0f0f0f0, v10
	v_perm_b32 v11, v26, v11, s33
	v_dot4c_i32_i8_e32 v88, s56, v10
	v_and_b32_e32 v10, 0xf0f0f0f0, v12
	v_dot4c_i32_i8_e32 v89, s56, v10
	v_and_b32_e32 v10, 0xf0f0f0f0, v11
	v_and_b32_e32 v26, 0xf0f0f0f0, v27
	v_dot4c_i32_i8_e32 v97, s56, v12
	v_dot4c_i32_i8_e32 v90, s56, v10
	v_perm_b32 v10, v29, v13, s67
	v_perm_b32 v12, v61, v45, s67
	v_dot4c_i32_i8_e32 v87, s56, v26
	v_dot4c_i32_i8_e32 v98, s56, v11
	v_perm_b32 v11, v29, v13, s68
	v_perm_b32 v13, v61, v45, s68
	v_perm_b32 v26, v12, v10, s69
	v_perm_b32 v10, v12, v10, s33
	v_perm_b32 v12, v13, v11, s69
	v_dot4c_i32_i8_e32 v100, s56, v10
	v_and_b32_e32 v10, 0xf0f0f0f0, v10
	v_perm_b32 v11, v13, v11, s33
	v_dot4c_i32_i8_e32 v92, s56, v10
	v_and_b32_e32 v10, 0xf0f0f0f0, v12
	s_add_i32 s91, s63, -7
	v_and_b32_e32 v13, 0xf0f0f0f0, v26
	v_dot4c_i32_i8_e32 v93, s56, v10
	v_and_b32_e32 v10, 0xf0f0f0f0, v11
	s_bitcmp0_b32 s91, 6
	v_dot4c_i32_i8_e32 v66, s56, v58
	v_dot4c_i32_i8_e32 v75, s56, v106
	v_dot4c_i32_i8_e32 v80, s56, v42
	v_dot4c_i32_i8_e32 v95, s56, v27
	v_dot4c_i32_i8_e32 v99, s56, v26
	v_dot4c_i32_i8_e32 v91, s56, v13
	v_dot4c_i32_i8_e32 v101, s56, v12
	v_dot4c_i32_i8_e32 v102, s56, v11
	v_dot4c_i32_i8_e32 v83, s56, v10
	s_cselect_b64 s[56:57], -1, 0
	v_cndmask_b32_e64 v10, v79, v78, s[56:57]
	v_cndmask_b32_e32 v10, v10, v199, vcc
	s_add_i32 s57, s90, 0xfff20000
	v_readlane_b32 s56, v10, s91
	s_lshl_b32 s56, s56, 10
	s_and_b32 s57, s57, 0x1000000
	s_add_i32 s56, s56, s57
	s_add_i32 s91, s63, -6
	s_bitcmp0_b32 s91, 6
	buffer_load_dwordx4 v[10:13], v0, s[92:95], s56 offen
	s_cselect_b64 s[56:57], -1, 0
	v_cndmask_b32_e64 v26, v79, v78, s[56:57]
	v_cndmask_b32_e32 v26, v26, v199, vcc
	s_add_i32 s57, s90, 0xfff40000
	v_readlane_b32 s56, v26, s91
	s_lshl_b32 s56, s56, 10
	s_and_b32 s57, s57, 0x1000000
	s_add_i32 s56, s56, s57
	s_add_i32 s91, s63, -5
	s_bitcmp0_b32 s91, 6
	buffer_load_dwordx4 v[26:29], v0, s[92:95], s56 offen
	s_cselect_b64 s[56:57], -1, 0
	v_cndmask_b32_e64 v42, v79, v78, s[56:57]
	v_cndmask_b32_e32 v42, v42, v199, vcc
	s_add_i32 s57, s90, 0xfff60000
	v_readlane_b32 s56, v42, s91
	s_lshl_b32 s56, s56, 10
	s_and_b32 s57, s57, 0x1000000
	s_add_i32 s56, s56, s57
	s_add_i32 s91, s63, -4
	s_bitcmp0_b32 s91, 6
	buffer_load_dwordx4 v[42:45], v0, s[92:95], s56 offen
	s_cselect_b64 s[56:57], -1, 0
	v_cndmask_b32_e64 v58, v79, v78, s[56:57]
	v_cndmask_b32_e32 v58, v58, v199, vcc
	s_add_i32 s57, s90, 0xfff80000
	v_readlane_b32 s56, v58, s91
	s_lshl_b32 s56, s56, 10
	s_and_b32 s57, s57, 0x1000000
	s_add_i32 s56, s56, s57
	s_nop 1
	buffer_load_dwordx4 v[58:61], v0, s[92:95], s56 offen
	s_add_i32 s56, s63, 0xffffff2d
	s_waitcnt vmcnt(5)
	v_perm_b32 v106, v34, v18, s67
	v_perm_b32 v18, v34, v18, s68
	s_waitcnt vmcnt(3)
	v_perm_b32 v34, v62, v50, s67
	v_readlane_b32 s56, v105, s56
	v_perm_b32 v50, v62, v50, s68
	v_perm_b32 v62, v34, v106, s69
	v_perm_b32 v34, v34, v106, s33
	v_perm_b32 v106, v50, v18, s69
	v_perm_b32 v18, v50, v18, s33
	v_dot4c_i32_i8_e32 v74, s56, v34
	v_and_b32_e32 v34, 0xf0f0f0f0, v34
	v_dot4c_i32_i8_e32 v70, s56, v34
	v_and_b32_e32 v34, 0xf0f0f0f0, v106
	v_dot4c_i32_i8_e32 v76, s56, v18
	v_and_b32_e32 v18, 0xf0f0f0f0, v18
	v_and_b32_e32 v50, 0xf0f0f0f0, v62
	v_dot4c_i32_i8_e32 v72, s56, v34
	v_dot4c_i32_i8_e32 v73, s56, v18
	v_perm_b32 v18, v35, v19, s67
	v_perm_b32 v34, v63, v51, s67
	v_dot4c_i32_i8_e32 v69, s56, v50
	v_perm_b32 v19, v35, v19, s68
	v_perm_b32 v35, v63, v51, s68
	v_perm_b32 v50, v34, v18, s69
	v_perm_b32 v18, v34, v18, s33
	v_perm_b32 v34, v35, v19, s69
	v_dot4c_i32_i8_e32 v85, s56, v18
	v_and_b32_e32 v18, 0xf0f0f0f0, v18
	v_perm_b32 v19, v35, v19, s33
	v_dot4c_i32_i8_e32 v81, s56, v18
	v_and_b32_e32 v18, 0xf0f0f0f0, v34
	v_dot4c_i32_i8_e32 v82, s56, v18
	v_and_b32_e32 v18, 0xf0f0f0f0, v19
	v_and_b32_e32 v35, 0xf0f0f0f0, v50
	v_dot4c_i32_i8_e32 v94, s56, v19
	v_dot4c_i32_i8_e32 v84, s56, v18
	v_perm_b32 v18, v36, v20, s67
	v_perm_b32 v19, v36, v20, s68
	v_perm_b32 v20, v64, v52, s67
	v_dot4c_i32_i8_e32 v77, s56, v35
	v_dot4c_i32_i8_e32 v86, s56, v34
	v_perm_b32 v34, v64, v52, s68
	v_perm_b32 v35, v20, v18, s69
	v_perm_b32 v18, v20, v18, s33
	v_perm_b32 v20, v34, v19, s69
	v_dot4c_i32_i8_e32 v96, s56, v18
	v_and_b32_e32 v18, 0xf0f0f0f0, v18
	v_perm_b32 v19, v34, v19, s33
	v_dot4c_i32_i8_e32 v88, s56, v18
	v_and_b32_e32 v18, 0xf0f0f0f0, v20
	v_dot4c_i32_i8_e32 v89, s56, v18
	v_and_b32_e32 v18, 0xf0f0f0f0, v19
	v_and_b32_e32 v34, 0xf0f0f0f0, v35
	v_dot4c_i32_i8_e32 v97, s56, v20
	v_dot4c_i32_i8_e32 v90, s56, v18
	v_perm_b32 v18, v37, v21, s67
	v_perm_b32 v20, v65, v53, s67
	v_dot4c_i32_i8_e32 v87, s56, v34
	v_dot4c_i32_i8_e32 v98, s56, v19
	v_perm_b32 v19, v37, v21, s68
	v_perm_b32 v21, v65, v53, s68
	v_perm_b32 v34, v20, v18, s69
	v_perm_b32 v18, v20, v18, s33
	v_perm_b32 v20, v21, v19, s69
	v_dot4c_i32_i8_e32 v100, s56, v18
	v_and_b32_e32 v18, 0xf0f0f0f0, v18
	v_perm_b32 v19, v21, v19, s33
	v_dot4c_i32_i8_e32 v92, s56, v18
	v_and_b32_e32 v18, 0xf0f0f0f0, v20
	s_add_i32 s91, s63, -3
	v_and_b32_e32 v21, 0xf0f0f0f0, v34
	v_dot4c_i32_i8_e32 v93, s56, v18
	v_and_b32_e32 v18, 0xf0f0f0f0, v19
	s_bitcmp0_b32 s91, 6
	v_dot4c_i32_i8_e32 v66, s56, v62
	v_dot4c_i32_i8_e32 v75, s56, v106
	v_dot4c_i32_i8_e32 v80, s56, v50
	v_dot4c_i32_i8_e32 v95, s56, v35
	v_dot4c_i32_i8_e32 v99, s56, v34
	v_dot4c_i32_i8_e32 v91, s56, v21
	v_dot4c_i32_i8_e32 v101, s56, v20
	v_dot4c_i32_i8_e32 v102, s56, v19
	v_dot4c_i32_i8_e32 v83, s56, v18
	s_cselect_b64 s[56:57], -1, 0
	v_cndmask_b32_e64 v18, v79, v78, s[56:57]
	v_cndmask_b32_e32 v18, v18, v199, vcc
	s_add_i32 s57, s90, 0xfffa0000
	v_readlane_b32 s56, v18, s91
	s_lshl_b32 s56, s56, 10
	s_and_b32 s57, s57, 0x1000000
	s_add_i32 s56, s56, s57
	s_add_i32 s91, s63, -2
	s_bitcmp0_b32 s91, 6
	buffer_load_dwordx4 v[18:21], v0, s[92:95], s56 offen
	s_cselect_b64 s[56:57], -1, 0
	v_cndmask_b32_e64 v34, v79, v78, s[56:57]
	v_cndmask_b32_e32 v34, v34, v199, vcc
	s_add_i32 s57, s90, 0xfffc0000
	v_readlane_b32 s56, v34, s91
	s_lshl_b32 s56, s56, 10
	s_and_b32 s57, s57, 0x1000000
	s_add_i32 s56, s56, s57
	s_add_i32 s91, s63, -1
	s_bitcmp0_b32 s91, 6
	buffer_load_dwordx4 v[34:37], v0, s[92:95], s56 offen
	s_cselect_b64 s[56:57], -1, 0
	v_cndmask_b32_e64 v50, v79, v78, s[56:57]
	v_cndmask_b32_e32 v50, v50, v199, vcc
	s_add_i32 s57, s90, 0xfffe0000
	v_readlane_b32 s56, v50, s91
	s_lshl_b32 s56, s56, 10
	s_and_b32 s57, s57, 0x1000000
	s_add_i32 s56, s56, s57
	s_bitcmp0_b32 s63, 6
	s_nop 0
	buffer_load_dwordx4 v[50:53], v0, s[92:95], s56 offen
	s_cselect_b64 s[56:57], -1, 0
	v_cndmask_b32_e64 v62, v79, v78, s[56:57]
	v_cndmask_b32_e32 v62, v62, v199, vcc
	s_and_b32 s57, s90, 0x1000000
	v_readlane_b32 s56, v62, s63
	s_lshl_b32 s56, s56, 10
	s_add_i32 s56, s56, s57
	s_nop 2
	buffer_load_dwordx4 v[62:65], v0, s[92:95], s56 offen
	s_add_i32 s62, s62, 1
	s_add_i32 s63, s63, 16
	s_add_i32 s90, s90, 0x200000
	s_cmpk_eq_i32 s63, 0x11f
	s_cbranch_scc0 .LBB0_1425
; __device__ __forceinline__ int ov(int x) { asm volatile("" : "+v"(x)); return x; }
; __device__ __forceinline__ int shl_i(int v, int from_lane) { return __builtin_amdgcn_ds_bpermute(from_lane << 2, v); }
;     ...
;         const int c8 = 8 * (int)wave_sum((float)(q0 + q1));
;         const int pk0 = (q0 & 0xFF) | ((shl_i(q0, lane + 1) & 0xFF) << 8) | ((shl_i(q0, lane + 2) & 0xFF) << 16) | (shl_i(q0, lane + 3) << 24);
;         const int pk1 = (q1 & 0xFF) | ((shl_i(q1, lane + 1) & 0xFF) << 8) | ((shl_i(q1, lane + 2) & 0xFF) << 16) | (shl_i(q1, lane + 3) << 24);
;         int acci[32];
; #pragma unroll
;         for (int i = 0; i < 32; ++i) acci[i] = 0;
;         GATHER_V_SECTION(2, pk0)
;         GATHER_V_SECTION(3, pk1)
;     ...
;         f32x2 acc[16];
;         { const float fsc = wm * (1.0f / 127.0f);
; #pragma unroll
;           for (int i = 0; i < 16; ++i) acc[i] = (f32x2){(float)(acci[2 * i] - acci[2 * i + 1] - c8) * fsc, (float)acci[2 * i + 1] * (fsc * 0.0625f)}; }
;         const int lane2 = ov(lane);
;         float s = 0.f;
; #pragma unroll
;         for (int hh = 0; hh < 4; ++hh) { float pl[8]; unpack8(*(const v4u*)(PLE + (size_t)t * D + lane2 * 32 + hh * 8), pl);
;             float z8[8]; unpack8(*(const v4u*)(ZB + (size_t)t * D + lane2 * 32 + hh * 8), z8);
;             f32x4 xa = (f32x4){z8[0], z8[1], z8[2], z8[3]}, xb = (f32x4){z8[4], z8[5], z8[6], z8[7]};
;             xa = (xa - mean1) * rstd1 * *(const f32x4*)(gain1 + lane2 * 32 + hh * 8) + *(const f32x4*)(bias1 + lane2 * 32 + hh * 8);
;             xb = (xb - mean1) * rstd1 * *(const f32x4*)(gain1 + lane2 * 32 + hh * 8 + 4) + *(const f32x4*)(bias1 + lane2 * 32 + hh * 8 + 4);
	s_waitcnt lgkmcnt(0)
	v_add_f32_e32 v78, v103, v104
	v_cvt_i32_f32_e32 v78, v78
	v_mov_b32_e32 v201, v130
	s_lshl_b64 s[56:57], s[86:87], 1
	v_lshlrev_b32_e32 v78, 3, v78
	v_sub_u32_e32 v78, 0, v78
	v_sub_u32_e32 v79, v78, v69
	v_add_u32_e32 v66, v79, v66
	v_sub_u32_e32 v79, v78, v70
	v_add_u32_e32 v74, v79, v74
	v_sub_u32_e32 v79, v78, v72
	v_add_u32_e32 v75, v79, v75
	v_sub_u32_e32 v79, v78, v73
	v_add_u32_e32 v76, v79, v76
	v_sub_u32_e32 v79, v78, v77
	v_add_u32_e32 v79, v79, v80
	v_sub_u32_e32 v80, v78, v81
	v_add_u32_e32 v80, v80, v85
	v_sub_u32_e32 v85, v78, v82
	v_add_u32_e32 v85, v85, v86
	v_sub_u32_e32 v86, v78, v84
	v_add_u32_e32 v86, v86, v94
	v_sub_u32_e32 v94, v78, v87
	v_add_u32_e32 v94, v94, v95
	v_sub_u32_e32 v95, v78, v88
	v_readlane_b32 s62, v255, 7
	v_lshlrev_b32_e32 v134, 5, v201
	v_add_u32_e32 v95, v95, v96
	v_sub_u32_e32 v96, v78, v89
	s_add_u32 s62, s62, s56
	v_readlane_b32 s63, v255, 9
	v_ashrrev_i32_e32 v135, 31, v134
	v_add_u32_e32 v96, v96, v97
	v_sub_u32_e32 v97, v78, v90
	v_cvt_f32_i32_e32 v181, v70
	v_mul_f32_e32 v142, 0x3c010204, v71
	s_addc_u32 s63, s63, s57
	v_lshlrev_b64 v[70:71], 1, v[134:135]
	v_add_u32_e32 v97, v97, v98
	v_sub_u32_e32 v98, v78, v91
	v_cvt_f32_i32_e32 v178, v75
	v_cvt_f32_i32_e32 v180, v74
	v_lshl_add_u64 v[74:75], s[62:63], 0, v[70:71]
	v_readlane_b32 s62, v254, 56
	v_add_u32_e32 v98, v98, v99
	v_sub_u32_e32 v99, v78, v92
	s_add_u32 s62, s62, s56
	v_readlane_b32 s63, v255, 5
	v_add_u32_e32 v99, v99, v100
	v_sub_u32_e32 v100, v78, v93
	v_sub_u32_e32 v78, v78, v83
	s_addc_u32 s63, s63, s57
	v_add_u32_e32 v100, v100, v101
	v_add_u32_e32 v78, v78, v102
	v_cvt_f32_i32_e32 v138, v99
	v_cvt_f32_i32_e32 v140, v98
	v_lshl_add_u64 v[98:99], s[62:63], 0, v[70:71]
	v_cvt_f32_i32_e32 v136, v100
	v_cvt_f32_i32_e32 v137, v93
	v_cvt_f32_i32_e32 v139, v92
	v_cvt_f32_i32_e32 v141, v91
	v_cvt_f32_i32_e32 v146, v97
	v_cvt_f32_i32_e32 v147, v90
	v_cvt_f32_i32_e32 v148, v96
	v_cvt_f32_i32_e32 v149, v89
	v_cvt_f32_i32_e32 v150, v95
	v_cvt_f32_i32_e32 v151, v88
	v_cvt_f32_i32_e32 v152, v94
	v_cvt_f32_i32_e32 v153, v87
	v_cvt_f32_i32_e32 v160, v86
	v_cvt_f32_i32_e32 v161, v84
	v_cvt_f32_i32_e32 v170, v85
	v_cvt_f32_i32_e32 v171, v82
	v_cvt_f32_i32_e32 v172, v80
	v_cvt_f32_i32_e32 v173, v81
	v_cvt_f32_i32_e32 v174, v79
	v_cvt_f32_i32_e32 v175, v77
	v_cvt_f32_i32_e32 v176, v76
	v_cvt_f32_i32_e32 v177, v73
	v_cvt_f32_i32_e32 v179, v72
	v_cvt_f32_i32_e32 v144, v78
	v_cvt_f32_i32_e32 v145, v83
	v_mov_b32_e32 v70, v212
	v_mov_b32_e32 v71, v213
	v_mov_b32_e32 v72, v214
	v_mov_b32_e32 v73, v215
	v_mov_b32_e32 v78, v216
	v_mov_b32_e32 v79, v217
	v_mov_b32_e32 v80, v218
	v_mov_b32_e32 v81, v219
	v_mov_b32_e32 v86, v220
	v_mov_b32_e32 v87, v221
	v_mov_b32_e32 v88, v222
	v_mov_b32_e32 v89, v223
	v_mov_b32_e32 v90, v224
	v_mov_b32_e32 v91, v225
	v_mov_b32_e32 v92, v226
	v_mov_b32_e32 v93, v227
	v_mov_b32_e32 v74, v228
	v_mov_b32_e32 v75, v229
	v_mov_b32_e32 v76, v230
	v_mov_b32_e32 v77, v231
	v_mov_b32_e32 v82, v232
	v_mov_b32_e32 v83, v233
	v_mov_b32_e32 v84, v234
	v_mov_b32_e32 v85, v235
	v_mov_b32_e32 v94, v236
	v_mov_b32_e32 v95, v237
	v_mov_b32_e32 v96, v238
	v_mov_b32_e32 v97, v239
	v_mov_b32_e32 v98, v240
	v_mov_b32_e32 v99, v241
	v_mov_b32_e32 v100, v242
	v_mov_b32_e32 v101, v243
	v_cvt_f32_i32_e32 v182, v66
	v_cvt_f32_i32_e32 v183, v69
	v_lshlrev_b64 v[154:155], 2, v[134:135]
	v_readlane_b32 s62, v255, 13
	v_lshl_add_u64 v[158:159], s[36:37], 0, v[154:155]
	v_readlane_b32 s63, v255, 14
	v_mul_f32_e32 v143, 0x3d800000, v142
	v_readlane_b32 s72, v254, 20
	v_lshl_add_u64 v[156:157], s[62:63], 0, v[154:155]
	v_readlane_b32 s73, v254, 21
	v_readlane_b32 s72, v255, 15
	v_readlane_b32 s73, v255, 16
	s_lshl_b64 s[62:63], s[86:87], 2
	v_readlane_b32 s74, v254, 22
	v_readlane_b32 s75, v254, 23
	s_add_u32 s62, s74, s62
	s_addc_u32 s63, s75, s63
	s_and_b64 vcc, exec, s[82:83]
	v_readlane_b32 s76, v254, 24
	v_readlane_b32 s77, v254, 25
	v_readlane_b32 s78, v254, 26
	v_readlane_b32 s79, v254, 27
	s_waitcnt vmcnt(0)
	v_readlane_b32 s98, v254, 58
	v_readlane_b32 s99, v255, 1
	s_cmp_lt_i32 s98, 0x4000
	s_cselect_b32 s100, s98, s88
	s_add_i32 s99, s98, s99
	s_cmp_lt_i32 s99, 0x4000
	s_cselect_b32 s99, s99, s100
	s_lshl_b32 s100, s100, 12
	s_lshl_b32 s99, s99, 9
	v_lshl_add_u32 v244, v130, 6, s100
	v_lshl_add_u32 v249, v130, 2, s99
	v_readlane_b32 s100, v255, 7
	v_readlane_b32 s101, v255, 9
	s_nop 4
	global_load_dwordx4 v[212:215], v244, s[100:101] offset:48
	global_load_dwordx4 v[216:219], v244, s[100:101] offset:32
	global_load_dwordx4 v[220:223], v244, s[100:101] offset:16
	global_load_dwordx4 v[224:227], v244, s[100:101]
	v_readlane_b32 s100, v254, 56
	v_readlane_b32 s101, v255, 5
	s_nop 4
	global_load_dwordx4 v[228:231], v244, s[100:101] offset:48
	global_load_dwordx4 v[232:235], v244, s[100:101] offset:32
	global_load_dwordx4 v[236:239], v244, s[100:101] offset:16
	global_load_dwordx4 v[240:243], v244, s[100:101]
	global_load_dword v245, v249, s[70:71] offset:256
	global_load_dword v246, v249, s[40:41] offset:256
	global_load_dword v247, v249, s[40:41]
	global_load_dword v248, v249, s[70:71]
	v_lshlrev_b32_e32 v66, 16, v98
	v_and_b32_e32 v69, 0xffff0000, v98
	v_lshlrev_b32_e32 v98, 16, v99
	v_and_b32_e32 v99, 0xffff0000, v99
	v_lshlrev_b32_e32 v164, 16, v100
	v_and_b32_e32 v165, 0xffff0000, v100
	v_lshlrev_b32_e32 v166, 16, v101
	v_and_b32_e32 v167, 0xffff0000, v101
	v_sub_f32_e32 v99, v99, v67
	v_sub_f32_e32 v98, v98, v67
	v_sub_f32_e32 v101, v69, v67
	v_sub_f32_e32 v100, v66, v67
	v_pk_mul_f32 v[184:185], v[68:69], v[100:101] op_sel_hi:[0,1]
	v_pk_mul_f32 v[186:187], v[68:69], v[98:99] op_sel_hi:[0,1]
	ds_read_b128 v[98:101], v154 offset:48
	ds_read_b128 v[102:105], v154 offset:32
	ds_read_b128 v[106:109], v154 offset:16
	ds_read_b128 v[122:125], v154 offset:0
	ds_read_b128 v[110:113], v154 offset:8240
	ds_read_b128 v[114:117], v154 offset:8224
	ds_read_b128 v[118:121], v154 offset:8208
	ds_read_b128 v[126:129], v154 offset:8192
	s_waitcnt lgkmcnt(0)
;     ...
;         for (int hh = 0; hh < 4; ++hh) { float pl[8]; unpack8(*(const v4u*)(PLE + (size_t)t * D + lane2 * 32 + hh * 8), pl);
;             float z8[8]; unpack8(*(const v4u*)(ZB + (size_t)t * D + lane2 * 32 + hh * 8), z8);
;             f32x4 xa = (f32x4){z8[0], z8[1], z8[2], z8[3]}, xb = (f32x4){z8[4], z8[5], z8[6], z8[7]};
;             xa = (xa - mean1) * rstd1 * *(const f32x4*)(gain1 + lane2 * 32 + hh * 8) + *(const f32x4*)(bias1 + lane2 * 32 + hh * 8);
;             xb = (xb - mean1) * rstd1 * *(const f32x4*)(gain1 + lane2 * 32 + hh * 8 + 4) + *(const f32x4*)(bias1 + lane2 * 32 + hh * 8 + 4);
;             acc[hh * 4 + 0] += (f32x2){ALPHA * xa[0] + pl[0], ALPHA * xa[1] + pl[1]}; acc[hh * 4 + 1] += (f32x2){ALPHA * xa[2] + pl[2], ALPHA * xa[3] + pl[3]};
;             acc[hh * 4 + 2] += (f32x2){ALPHA * xb[0] + pl[4], ALPHA * xb[1] + pl[5]}; acc[hh * 4 + 3] += (f32x2){ALPHA * xb[2] + pl[6], ALPHA * xb[3] + pl[7]};
; #pragma unroll
;             for (int i = 0; i < 4; ++i) s += acc[hh * 4 + i].x + acc[hh * 4 + i].y; }
	v_pk_fma_f32 v[124:125], v[124:125], v[186:187], v[128:129]
	v_sub_f32_e32 v129, v165, v67
	v_sub_f32_e32 v128, v164, v67
	v_pk_mul_f32 v[128:129], v[68:69], v[128:129] op_sel_hi:[0,1]
	v_pk_fma_f32 v[122:123], v[122:123], v[184:185], v[126:127]
	v_sub_f32_e32 v127, v167, v67
	v_sub_f32_e32 v126, v166, v67
	v_pk_fma_f32 v[106:107], v[106:107], v[128:129], v[118:119]
	v_lshlrev_b32_e32 v118, 16, v90
	v_and_b32_e32 v119, 0xffff0000, v90
	v_lshlrev_b32_e32 v90, 16, v91
	v_and_b32_e32 v91, 0xffff0000, v91
	v_pk_mul_f32 v[126:127], v[68:69], v[126:127] op_sel_hi:[0,1]
	v_pk_fma_f32 v[90:91], v[124:125], s[58:59], v[90:91] op_sel_hi:[1,0,1]
	v_pk_fma_f32 v[108:109], v[108:109], v[126:127], v[120:121]
	v_pk_fma_f32 v[118:119], v[122:123], s[58:59], v[118:119] op_sel_hi:[1,0,1]
	v_pk_fma_f32 v[120:121], v[142:143], v[180:181], v[90:91]
	v_lshlrev_b32_e32 v90, 16, v92
	v_and_b32_e32 v91, 0xffff0000, v92
	v_pk_fma_f32 v[118:119], v[142:143], v[182:183], v[118:119]
	v_pk_fma_f32 v[90:91], v[106:107], s[58:59], v[90:91] op_sel_hi:[1,0,1]
	v_add_f32_e32 v66, v118, v119
	v_pk_fma_f32 v[122:123], v[142:143], v[178:179], v[90:91]
	v_lshlrev_b32_e32 v90, 16, v93
	v_and_b32_e32 v91, 0xffff0000, v93
	v_pk_fma_f32 v[90:91], v[108:109], s[58:59], v[90:91] op_sel_hi:[1,0,1]
	v_add_f32_e32 v66, 0, v66
	v_add_f32_e32 v69, v120, v121
	v_pk_fma_f32 v[124:125], v[142:143], v[176:177], v[90:91]
	v_add_f32_e32 v66, v69, v66
	v_add_f32_e32 v69, v122, v123
	v_add_f32_e32 v66, v69, v66
	v_add_f32_e32 v69, v124, v125
	v_lshlrev_b32_e32 v90, 16, v95
	v_and_b32_e32 v91, 0xffff0000, v95
	v_lshlrev_b32_e32 v106, 16, v96
	v_and_b32_e32 v96, 0xffff0000, v96
	v_add_f32_e32 v66, v69, v66
	v_lshlrev_b32_e32 v69, 16, v94
	v_and_b32_e32 v92, 0xffff0000, v94
	v_lshlrev_b32_e32 v94, 16, v97
	v_and_b32_e32 v95, 0xffff0000, v97
	v_sub_f32_e32 v91, v91, v67
	v_sub_f32_e32 v90, v90, v67
	v_sub_f32_e32 v97, v96, v67
	v_sub_f32_e32 v96, v106, v67
	v_sub_f32_e32 v93, v92, v67
	v_sub_f32_e32 v92, v69, v67
	v_pk_mul_f32 v[90:91], v[68:69], v[90:91] op_sel_hi:[0,1]
	v_pk_mul_f32 v[96:97], v[68:69], v[96:97] op_sel_hi:[0,1]
	v_pk_mul_f32 v[92:93], v[68:69], v[92:93] op_sel_hi:[0,1]
	v_pk_fma_f32 v[90:91], v[104:105], v[90:91], v[116:117]
	v_pk_fma_f32 v[96:97], v[98:99], v[96:97], v[110:111]
	v_lshlrev_b32_e32 v98, 16, v86
	v_and_b32_e32 v99, 0xffff0000, v86
	v_lshlrev_b32_e32 v86, 16, v87
	v_and_b32_e32 v87, 0xffff0000, v87
	v_pk_fma_f32 v[92:93], v[102:103], v[92:93], v[114:115]
	v_pk_fma_f32 v[86:87], v[90:91], s[58:59], v[86:87] op_sel_hi:[1,0,1]
	v_sub_f32_e32 v95, v95, v67
	v_sub_f32_e32 v94, v94, v67
	v_pk_fma_f32 v[92:93], v[92:93], s[58:59], v[98:99] op_sel_hi:[1,0,1]
	v_pk_fma_f32 v[116:117], v[142:143], v[172:173], v[86:87]
	v_lshlrev_b32_e32 v86, 16, v88
	v_and_b32_e32 v87, 0xffff0000, v88
	v_pk_mul_f32 v[94:95], v[68:69], v[94:95] op_sel_hi:[0,1]
	v_pk_fma_f32 v[114:115], v[142:143], v[174:175], v[92:93]
	v_pk_fma_f32 v[86:87], v[96:97], s[58:59], v[86:87] op_sel_hi:[1,0,1]
	v_pk_fma_f32 v[94:95], v[100:101], v[94:95], v[112:113]
	v_pk_fma_f32 v[126:127], v[142:143], v[170:171], v[86:87]
	v_lshlrev_b32_e32 v86, 16, v89
	v_and_b32_e32 v87, 0xffff0000, v89
	v_add_f32_e32 v69, v114, v115
	v_pk_fma_f32 v[86:87], v[94:95], s[58:59], v[86:87] op_sel_hi:[1,0,1]
	v_add_f32_e32 v66, v66, v69
	v_add_f32_e32 v69, v116, v117
	v_pk_fma_f32 v[128:129], v[142:143], v[160:161], v[86:87]
	v_add_f32_e32 v66, v69, v66
	v_add_f32_e32 v69, v126, v127
	v_add_f32_e32 v66, v69, v66
	v_add_f32_e32 v69, v128, v129
	v_lshlrev_b32_e32 v86, 16, v82
	v_and_b32_e32 v87, 0xffff0000, v82
	v_lshlrev_b32_e32 v82, 16, v83
	v_and_b32_e32 v83, 0xffff0000, v83
	v_add_f32_e32 v66, v69, v66
	v_lshlrev_b32_e32 v69, 16, v84
	v_and_b32_e32 v172, 0xffff0000, v84
	v_lshlrev_b32_e32 v173, 16, v85
	v_and_b32_e32 v174, 0xffff0000, v85
	v_sub_f32_e32 v83, v83, v67
	v_sub_f32_e32 v82, v82, v67
	v_sub_f32_e32 v85, v87, v67
	v_sub_f32_e32 v84, v86, v67
	v_pk_mul_f32 v[160:161], v[68:69], v[84:85] op_sel_hi:[0,1]
	v_pk_mul_f32 v[170:171], v[68:69], v[82:83] op_sel_hi:[0,1]
	ds_read_b128 v[82:85], v154 offset:112
	ds_read_b128 v[86:89], v154 offset:96
	ds_read_b128 v[90:93], v154 offset:80
	ds_read_b128 v[106:109], v154 offset:64
	ds_read_b128 v[94:97], v154 offset:8304
	ds_read_b128 v[98:101], v154 offset:8288
	ds_read_b128 v[102:105], v154 offset:8272
	ds_read_b128 v[110:113], v154 offset:8256
	s_waitcnt lgkmcnt(0)
;     ...
;         for (int hh = 0; hh < 4; ++hh) { float pl[8]; unpack8(*(const v4u*)(PLE + (size_t)t * D + lane2 * 32 + hh * 8), pl);
;             float z8[8]; unpack8(*(const v4u*)(ZB + (size_t)t * D + lane2 * 32 + hh * 8), z8);
;             f32x4 xa = (f32x4){z8[0], z8[1], z8[2], z8[3]}, xb = (f32x4){z8[4], z8[5], z8[6], z8[7]};
;             xa = (xa - mean1) * rstd1 * *(const f32x4*)(gain1 + lane2 * 32 + hh * 8) + *(const f32x4*)(bias1 + lane2 * 32 + hh * 8);
;             xb = (xb - mean1) * rstd1 * *(const f32x4*)(gain1 + lane2 * 32 + hh * 8 + 4) + *(const f32x4*)(bias1 + lane2 * 32 + hh * 8 + 4);
;             acc[hh * 4 + 0] += (f32x2){ALPHA * xa[0] + pl[0], ALPHA * xa[1] + pl[1]}; acc[hh * 4 + 1] += (f32x2){ALPHA * xa[2] + pl[2], ALPHA * xa[3] + pl[3]};
;             acc[hh * 4 + 2] += (f32x2){ALPHA * xb[0] + pl[4], ALPHA * xb[1] + pl[5]}; acc[hh * 4 + 3] += (f32x2){ALPHA * xb[2] + pl[6], ALPHA * xb[3] + pl[7]};
; #pragma unroll
;             for (int i = 0; i < 4; ++i) s += acc[hh * 4 + i].x + acc[hh * 4 + i].y; }
;         const float mean = wave_sum(s) * (1.0f / D); float q = 0.f;
	v_pk_fma_f32 v[108:109], v[108:109], v[170:171], v[112:113]
	v_sub_f32_e32 v113, v172, v67
	v_sub_f32_e32 v112, v69, v67
	v_pk_mul_f32 v[112:113], v[68:69], v[112:113] op_sel_hi:[0,1]
	v_pk_fma_f32 v[106:107], v[106:107], v[160:161], v[110:111]
	v_sub_f32_e32 v111, v174, v67
	v_sub_f32_e32 v110, v173, v67
	v_pk_fma_f32 v[90:91], v[90:91], v[112:113], v[102:103]
	v_lshlrev_b32_e32 v102, 16, v78
	v_and_b32_e32 v103, 0xffff0000, v78
	v_lshlrev_b32_e32 v78, 16, v79
	v_and_b32_e32 v79, 0xffff0000, v79
	v_pk_mul_f32 v[110:111], v[68:69], v[110:111] op_sel_hi:[0,1]
	v_pk_fma_f32 v[78:79], v[108:109], s[58:59], v[78:79] op_sel_hi:[1,0,1]
	v_pk_fma_f32 v[92:93], v[92:93], v[110:111], v[104:105]
	v_pk_fma_f32 v[102:103], v[106:107], s[58:59], v[102:103] op_sel_hi:[1,0,1]
	v_pk_fma_f32 v[104:105], v[142:143], v[150:151], v[78:79]
	v_lshlrev_b32_e32 v78, 16, v80
	v_and_b32_e32 v79, 0xffff0000, v80
	v_pk_fma_f32 v[102:103], v[142:143], v[152:153], v[102:103]
	v_pk_fma_f32 v[78:79], v[90:91], s[58:59], v[78:79] op_sel_hi:[1,0,1]
	v_add_f32_e32 v69, v102, v103
	v_pk_fma_f32 v[90:91], v[142:143], v[148:149], v[78:79]
	v_lshlrev_b32_e32 v78, 16, v81
	v_and_b32_e32 v79, 0xffff0000, v81
	v_pk_fma_f32 v[78:79], v[92:93], s[58:59], v[78:79] op_sel_hi:[1,0,1]
	v_add_f32_e32 v66, v66, v69
	v_add_f32_e32 v69, v104, v105
	v_pk_fma_f32 v[92:93], v[142:143], v[146:147], v[78:79]
	v_add_f32_e32 v66, v69, v66
	v_add_f32_e32 v69, v90, v91
	v_add_f32_e32 v66, v69, v66
	v_add_f32_e32 v69, v92, v93
	v_add_f32_e32 v106, v69, v66
	v_lshlrev_b32_e32 v66, 16, v74
	v_and_b32_e32 v69, 0xffff0000, v74
	v_lshlrev_b32_e32 v74, 16, v75
	v_and_b32_e32 v75, 0xffff0000, v75
	v_lshlrev_b32_e32 v80, 16, v76
	v_and_b32_e32 v81, 0xffff0000, v76
	v_lshlrev_b32_e32 v78, 16, v77
	v_and_b32_e32 v79, 0xffff0000, v77
	v_sub_f32_e32 v75, v75, v67
	v_sub_f32_e32 v74, v74, v67
	v_sub_f32_e32 v77, v69, v67
	v_sub_f32_e32 v76, v66, v67
	v_pk_mul_f32 v[74:75], v[68:69], v[74:75] op_sel_hi:[0,1]
	v_sub_f32_e32 v79, v79, v67
	v_sub_f32_e32 v78, v78, v67
	v_sub_f32_e32 v81, v81, v67
	v_sub_f32_e32 v80, v80, v67
	v_pk_mul_f32 v[76:77], v[68:69], v[76:77] op_sel_hi:[0,1]
	v_pk_fma_f32 v[74:75], v[88:89], v[74:75], v[100:101]
	v_pk_mul_f32 v[66:67], v[68:69], v[80:81] op_sel_hi:[0,1]
	v_pk_mul_f32 v[68:69], v[68:69], v[78:79] op_sel_hi:[0,1]
	v_lshlrev_b32_e32 v78, 16, v70
	v_and_b32_e32 v79, 0xffff0000, v70
	v_lshlrev_b32_e32 v70, 16, v71
	v_and_b32_e32 v71, 0xffff0000, v71
	v_pk_fma_f32 v[76:77], v[86:87], v[76:77], v[98:99]
	v_pk_fma_f32 v[70:71], v[74:75], s[58:59], v[70:71] op_sel_hi:[1,0,1]
	v_pk_fma_f32 v[68:69], v[84:85], v[68:69], v[96:97]
	v_pk_fma_f32 v[66:67], v[82:83], v[66:67], v[94:95]
	v_pk_fma_f32 v[76:77], v[76:77], s[58:59], v[78:79] op_sel_hi:[1,0,1]
	v_pk_fma_f32 v[96:97], v[142:143], v[138:139], v[70:71]
	v_lshlrev_b32_e32 v70, 16, v72
	v_and_b32_e32 v71, 0xffff0000, v72
	v_pk_fma_f32 v[94:95], v[142:143], v[140:141], v[76:77]
	v_pk_fma_f32 v[66:67], v[66:67], s[58:59], v[70:71] op_sel_hi:[1,0,1]
	v_lshlrev_b32_e32 v70, 16, v73
	v_and_b32_e32 v71, 0xffff0000, v73
	v_pk_fma_f32 v[68:69], v[68:69], s[58:59], v[70:71] op_sel_hi:[1,0,1]
	v_mov_b32_e32 v70, v96
	v_mov_b32_e32 v71, v94
	v_mov_b32_e32 v72, v97
	v_mov_b32_e32 v73, v95
	v_pk_add_f32 v[70:71], v[70:71], v[72:73]
	v_pk_fma_f32 v[66:67], v[142:143], v[136:137], v[66:67]
	v_pk_fma_f32 v[68:69], v[142:143], v[144:145], v[68:69]
	v_add_f32_e32 v71, v106, v71
	v_add_f32_e32 v74, v70, v71
	v_mov_b32_e32 v70, v68
	v_mov_b32_e32 v71, v66
	v_mov_b32_e32 v72, v69
	v_mov_b32_e32 v73, v67
	v_pk_add_f32 v[70:71], v[70:71], v[72:73]
	v_lshl_add_u64 v[100:101], s[72:73], 0, v[154:155]
	v_add_f32_e32 v71, v71, v74
	v_add_f32_e32 v70, v70, v71
	v_mov_b32_e32 v71, v1
	v_lshl_add_u64 v[98:99], s[62:63], 0, v[154:155]
	v_mbcnt_lo_u32_b32 v71, -1, v71
	v_mbcnt_hi_u32_b32 v71, -1, v71
	v_lshlrev_b32_e32 v71, 2, v71
	v_xor_b32_e32 v72, 0x80, v71
	ds_bpermute_b32 v72, v72, v70
	s_waitcnt lgkmcnt(0)
	v_add_f32_e32 v70, v70, v72
	v_xor_b32_e32 v72, 64, v71
	ds_bpermute_b32 v72, v72, v70
	s_waitcnt lgkmcnt(0)
	v_add_f32_e32 v70, v70, v72
	v_xor_b32_e32 v72, 32, v71
	ds_bpermute_b32 v72, v72, v70
	s_waitcnt lgkmcnt(0)
	v_add_f32_e32 v70, v70, v72
	v_xor_b32_e32 v72, 16, v71
	ds_bpermute_b32 v72, v72, v70
	s_waitcnt lgkmcnt(0)
	v_add_f32_e32 v70, v70, v72
	v_xor_b32_e32 v72, 8, v71
	ds_bpermute_b32 v72, v72, v70
	v_xor_b32_e32 v71, 4, v71
	s_waitcnt lgkmcnt(0)
	v_add_f32_e32 v70, v70, v72
	ds_bpermute_b32 v71, v71, v70
	s_waitcnt lgkmcnt(0)
; __device__ __forceinline__ float ln_rstd(float q) { return __builtin_amdgcn_rsqf((q + LN_EPS * (float)D) * (1.0f / D)); }
;     ...
;         const float mean = wave_sum(s) * (1.0f / D); float q = 0.f;
; #pragma unroll
;         for (int i = 0; i < 16; ++i) { acc[i].x -= mean; acc[i].y -= mean; q += acc[i].x * acc[i].x + acc[i].y * acc[i].y; }
;         const float rstd = ln_rstd(wave_sum(q));
; #pragma unroll
;         for (int hh = 0; hh < 4; ++hh) {
;             const int c = lane2 * 32 + hh * 8;
;             float y[8];
; #pragma unroll
;             for (int q4 = 0; q4 < 2; ++q4) { const f32x4 ga = *(const f32x4*)(gain + c + q4 * 4), ba = *(const f32x4*)(bias + c + q4 * 4);
;                 const f32x2 z0 = acc[hh * 4 + q4 * 2], z1 = acc[hh * 4 + q4 * 2 + 1];
;                 f32x4 yo; yo[0] = z0.x * rstd * ga[0] + ba[0]; yo[1] = z0.y * rstd * ga[1] + ba[1]; yo[2] = z1.x * rstd * ga[2] + ba[2]; yo[3] = z1.y * rstd * ga[3] + ba[3];
;                 if (OF) *(f32x4*)(OF + (size_t)t * D + c + q4 * 4) = yo;
	v_add_f32_e32 v70, v70, v71
	v_mul_f32_e32 v110, 0x3a000000, v70
	v_pk_add_f32 v[86:87], v[90:91], v[110:111] op_sel_hi:[1,0] neg_lo:[0,1] neg_hi:[0,1]
	v_pk_add_f32 v[88:89], v[92:93], v[110:111] op_sel_hi:[1,0] neg_lo:[0,1] neg_hi:[0,1]
	v_pk_add_f32 v[90:91], v[94:95], v[110:111] op_sel_hi:[1,0] neg_lo:[0,1] neg_hi:[0,1]
	v_pk_add_f32 v[92:93], v[96:97], v[110:111] op_sel_hi:[1,0] neg_lo:[0,1] neg_hi:[0,1]
	v_pk_add_f32 v[96:97], v[66:67], v[110:111] op_sel_hi:[1,0] neg_lo:[0,1] neg_hi:[0,1]
	v_pk_add_f32 v[94:95], v[68:69], v[110:111] op_sel_hi:[1,0] neg_lo:[0,1] neg_hi:[0,1]
	v_mov_b32_e32 v69, v97
	v_mov_b32_e32 v68, v95
	v_mov_b32_e32 v66, v94
	v_mov_b32_e32 v67, v96
	v_pk_mul_f32 v[68:69], v[68:69], v[68:69]
	v_pk_add_f32 v[82:83], v[102:103], v[110:111] op_sel_hi:[1,0] neg_lo:[0,1] neg_hi:[0,1]
	v_pk_fma_f32 v[144:145], v[66:67], v[66:67], v[68:69]
	v_mov_b32_e32 v66, v1
	v_lshl_add_u64 v[102:103], s[80:81], 0, v[154:155]
	v_mbcnt_lo_u32_b32 v66, -1, v66
	v_mbcnt_hi_u32_b32 v66, -1, v66
	v_lshlrev_b32_e32 v66, 2, v66
	v_xor_b32_e32 v148, 0x80, v66
	v_xor_b32_e32 v149, 64, v66
	v_xor_b32_e32 v150, 32, v66
	v_xor_b32_e32 v151, 16, v66
	v_xor_b32_e32 v152, 8, v66
	v_xor_b32_e32 v153, 4, v66
	ds_read_b128 v[66:69], v154 offset:16384
	ds_read_b128 v[106:109], v154 offset:24576
	v_pk_add_f32 v[70:71], v[122:123], v[110:111] op_sel_hi:[1,0] neg_lo:[0,1] neg_hi:[0,1]
	v_pk_add_f32 v[72:73], v[124:125], v[110:111] op_sel_hi:[1,0] neg_lo:[0,1] neg_hi:[0,1]
	v_pk_add_f32 v[74:75], v[114:115], v[110:111] op_sel_hi:[1,0] neg_lo:[0,1] neg_hi:[0,1]
	v_pk_add_f32 v[76:77], v[116:117], v[110:111] op_sel_hi:[1,0] neg_lo:[0,1] neg_hi:[0,1]
	v_pk_add_f32 v[78:79], v[126:127], v[110:111] op_sel_hi:[1,0] neg_lo:[0,1] neg_hi:[0,1]
	v_pk_add_f32 v[80:81], v[128:129], v[110:111] op_sel_hi:[1,0] neg_lo:[0,1] neg_hi:[0,1]
	v_pk_add_f32 v[84:85], v[104:105], v[110:111] op_sel_hi:[1,0] neg_lo:[0,1] neg_hi:[0,1]
	v_pk_add_f32 v[118:119], v[118:119], v[110:111] op_sel_hi:[1,0] neg_lo:[0,1] neg_hi:[0,1]
	v_pk_add_f32 v[110:111], v[120:121], v[110:111] op_sel_hi:[1,0] neg_lo:[0,1] neg_hi:[0,1]
	v_pk_mul_f32 v[146:147], v[118:119], v[118:119]
	v_pk_mul_f32 v[120:121], v[110:111], v[110:111]
	v_pk_mul_f32 v[112:113], v[70:71], v[70:71]
	v_add_f32_e32 v120, v120, v121
	v_add_f32_e32 v121, v146, v147
	v_pk_mul_f32 v[122:123], v[72:73], v[72:73]
	v_add_f32_e32 v120, v121, v120
	v_add_f32_e32 v112, v112, v113
	v_pk_mul_f32 v[114:115], v[74:75], v[74:75]
	v_add_f32_e32 v112, v112, v120
	v_add_f32_e32 v113, v122, v123
	v_pk_mul_f32 v[116:117], v[76:77], v[76:77]
	v_add_f32_e32 v112, v113, v112
	v_add_f32_e32 v113, v114, v115
	v_pk_mul_f32 v[124:125], v[78:79], v[78:79]
	v_add_f32_e32 v112, v113, v112
	v_add_f32_e32 v113, v116, v117
	v_pk_mul_f32 v[126:127], v[80:81], v[80:81]
	v_add_f32_e32 v112, v113, v112
	v_add_f32_e32 v113, v124, v125
	v_pk_mul_f32 v[128:129], v[82:83], v[82:83]
	v_add_f32_e32 v112, v113, v112
	v_add_f32_e32 v113, v126, v127
	v_pk_mul_f32 v[104:105], v[84:85], v[84:85]
	v_add_f32_e32 v112, v113, v112
	v_add_f32_e32 v113, v128, v129
	v_pk_mul_f32 v[136:137], v[86:87], v[86:87]
	v_add_f32_e32 v112, v113, v112
	v_add_f32_e32 v104, v104, v105
	v_pk_mul_f32 v[138:139], v[88:89], v[88:89]
	v_add_f32_e32 v104, v104, v112
	v_add_f32_e32 v105, v136, v137
	v_pk_mul_f32 v[140:141], v[90:91], v[90:91]
	v_add_f32_e32 v104, v105, v104
	v_add_f32_e32 v105, v138, v139
	v_pk_mul_f32 v[142:143], v[92:93], v[92:93]
	v_add_f32_e32 v104, v105, v104
	v_add_f32_e32 v105, v140, v141
	v_add_f32_e32 v104, v105, v104
	v_add_f32_e32 v105, v142, v143
	v_add_f32_e32 v104, v105, v104
	v_add_f32_e32 v104, v145, v104
	v_add_f32_e32 v104, v144, v104
	ds_bpermute_b32 v105, v148, v104
	s_waitcnt lgkmcnt(0)
	v_add_f32_e32 v104, v104, v105
	ds_bpermute_b32 v105, v149, v104
	s_waitcnt lgkmcnt(0)
	v_add_f32_e32 v104, v104, v105
	ds_bpermute_b32 v105, v150, v104
	s_waitcnt lgkmcnt(0)
	v_add_f32_e32 v104, v104, v105
	ds_bpermute_b32 v105, v151, v104
	s_waitcnt lgkmcnt(0)
	v_add_f32_e32 v104, v104, v105
	ds_bpermute_b32 v105, v152, v104
	s_waitcnt lgkmcnt(0)
	v_add_f32_e32 v104, v104, v105
	ds_bpermute_b32 v105, v153, v104
	s_waitcnt lgkmcnt(0)
	v_add_f32_e32 v104, v104, v105
	v_add_f32_e32 v104, 0x3ca7c5ac, v104
	v_mul_f32_e32 v104, 0x3a000000, v104
	v_rsq_f32_e32 v104, v104
	s_nop 0
	v_pk_mul_f32 v[112:113], v[118:119], v[104:105] op_sel_hi:[1,0]
	s_nop 0
	v_pk_fma_f32 v[66:67], v[66:67], v[112:113], v[106:107]
	v_pk_mul_f32 v[106:107], v[110:111], v[104:105] op_sel_hi:[1,0]
	s_nop 0
	v_pk_fma_f32 v[68:69], v[68:69], v[106:107], v[108:109]
	s_cbranch_vccz .LBB0_1428
	global_store_dwordx4 v[98:99], v[66:69], off

; __global__ void __launch_bounds__(NTHREADS, 2) mk_fwd(Args args) {
	.amdhsa_kernel _ZN2mk6mk_fwdENS_4ArgsE
		.amdhsa_group_segment_fixed_size 0
		.amdhsa_private_segment_fixed_size 0
		.amdhsa_kernarg_size 416
		.amdhsa_user_sgpr_count 2
		.amdhsa_user_sgpr_dispatch_ptr 0
		.amdhsa_user_sgpr_queue_ptr 0
		.amdhsa_user_sgpr_kernarg_segment_ptr 1
		.amdhsa_user_sgpr_dispatch_id 0
		.amdhsa_user_sgpr_kernarg_preload_length 0
		.amdhsa_user_sgpr_kernarg_preload_offset 0
		.amdhsa_user_sgpr_private_segment_size 0
		.amdhsa_uses_dynamic_stack 0
		.amdhsa_enable_private_segment 0
		.amdhsa_system_sgpr_workgroup_id_x 1
		.amdhsa_system_sgpr_workgroup_id_y 0
		.amdhsa_system_sgpr_workgroup_id_z 0
		.amdhsa_system_sgpr_workgroup_info 0
		.amdhsa_system_vgpr_workitem_id 0
		.amdhsa_next_free_vgpr 256
		.amdhsa_next_free_sgpr 102
		.amdhsa_accum_offset 256
		.amdhsa_reserve_vcc 1
		.amdhsa_float_round_mode_32 0
		.amdhsa_float_round_mode_16_64 0
		.amdhsa_float_denorm_mode_32 3
		.amdhsa_float_denorm_mode_16_64 3
		.amdhsa_dx10_clamp 1
		.amdhsa_ieee_mode 1
		.amdhsa_fp16_overflow 0
		.amdhsa_tg_split 0
		.amdhsa_exception_fp_ieee_invalid_op 0
		.amdhsa_exception_fp_denorm_src 0
		.amdhsa_exception_fp_ieee_div_zero 0
		.amdhsa_exception_fp_ieee_overflow 0
		.amdhsa_exception_fp_ieee_underflow 0
		.amdhsa_exception_fp_ieee_inexact 0
		.amdhsa_exception_int_div_zero 0
	.end_amdhsa_kernel

; __global__ void __launch_bounds__(NTHREADS, 2) mk_fwd(Args args) {
amdhsa.kernels:
  - .agpr_count:     0
    .args:
      - .offset:         0
        .size:           160
        .value_kind:     by_value
      - .offset:         160
        .size:           4
        .value_kind:     hidden_block_count_x
      - .offset:         164
        .size:           4
        .value_kind:     hidden_block_count_y
      - .offset:         168
        .size:           4
        .value_kind:     hidden_block_count_z
      - .offset:         172
        .size:           2
        .value_kind:     hidden_group_size_x
      - .offset:         174
        .size:           2
        .value_kind:     hidden_group_size_y
      - .offset:         176
        .size:           2
        .value_kind:     hidden_group_size_z
      - .offset:         178
        .size:           2
        .value_kind:     hidden_remainder_x
      - .offset:         180
        .size:           2
        .value_kind:     hidden_remainder_y
      - .offset:         182
        .size:           2
        .value_kind:     hidden_remainder_z
      - .offset:         200
        .size:           8
        .value_kind:     hidden_global_offset_x
      - .offset:         208
        .size:           8
        .value_kind:     hidden_global_offset_y
      - .offset:         216
        .size:           8
        .value_kind:     hidden_global_offset_z
      - .offset:         224
        .size:           2
        .value_kind:     hidden_grid_dims
      - .offset:         280
        .size:           4
        .value_kind:     hidden_dynamic_lds_size
    .group_segment_fixed_size: 0
    .kernarg_segment_align: 8
    .kernarg_segment_size: 416
    .language:       OpenCL C
    .language_version:
      - 2
      - 0
    .max_flat_workgroup_size: 512
    .name:           _ZN2mk6mk_fwdENS_4ArgsE
    .private_segment_fixed_size: 0
    .sgpr_count:     108
    .sgpr_spill_count: 230
    .symbol:         _ZN2mk6mk_fwdENS_4ArgsE.kd
    .uniform_work_group_size: 1
    .uses_dynamic_stack: false
    .vgpr_count:     256
    .vgpr_spill_count: 0
    .wavefront_size: 64
